# stack2: two-row modulate0, NAT prefetch counted waits, scatter epilogue waits, barrier polls top generation word
# baseline (speedup 1.0000x reference)
.LBB0_386:
	ds_read_b128 v[168:171], v159
	ds_read_b128 v[172:175], v159 offset:1024
	ds_read_b128 v[176:179], v159 offset:2048
	ds_read_b128 v[180:183], v159 offset:3072
	ds_read_b128 v[184:187], v160
	ds_read_b128 v[188:191], v160 offset:1024
	ds_read_b128 v[192:195], v160 offset:2048
	ds_read_b128 v[196:199], v160 offset:3072
	s_add_u32 s34, s84, s30
	s_addc_u32 s35, s85, s31
	s_add_u32 s36, s34, 0x25300100
	s_addc_u32 s37, s35, 0
	s_add_u32 s53, s27, s30
	s_addc_u32 s54, s29, s31
	s_cmpk_eq_i32 s30, 0xf00
	s_cselect_b64 vcc, -1, 0
	s_and_b64 s[34:35], vcc, exec
	v_cndmask_b32_e32 v134, v143, v163, vcc
	s_cselect_b32 s37, s9, s37
	s_cselect_b32 s36, s8, s36
	v_cndmask_b32_e32 v145, v146, v164, vcc
	v_cndmask_b32_e32 v212, v144, v165, vcc
	v_cndmask_b32_e32 v147, v148, v166, vcc
	s_cselect_b32 s35, s7, s54
	s_cselect_b32 s34, s6, s53
	v_lshl_add_u64 v[214:215], v[152:153], 0, s[30:31]
	s_add_i32 m0, s39, 0xc000
	ds_read_b128 v[200:203], v161
	ds_read_b128 v[204:207], v161 offset:1024
	ds_read_b128 v[208:211], v161 offset:2048
	ds_read_b128 v[216:219], v161 offset:3072
	ds_read_b128 v[220:223], v161 offset:4096
	ds_read_b128 v[224:227], v161 offset:5120
	ds_read_b128 v[228:231], v161 offset:6144
	ds_read_b128 v[232:235], v161 offset:7168
	global_load_lds_dwordx4 v[214:215], off
	v_lshl_add_u64 v[214:215], v[150:151], 0, s[30:31]
	s_add_i32 m0, s39, 0xe000
	s_nop 0
	global_load_lds_dwordx4 v[214:215], off
	s_waitcnt vmcnt(8)
	s_waitcnt lgkmcnt(0)
	s_barrier
	s_setprio 1
	s_waitcnt lgkmcnt(0)
	v_mfma_f32_16x16x32_bf16 v[126:129], v[168:171], v[200:203], v[126:129]
	v_mfma_f32_16x16x32_bf16 v[122:125], v[176:179], v[200:203], v[122:125]
	v_mfma_f32_16x16x32_bf16 v[118:121], v[168:171], v[208:211], v[118:121]
	v_mfma_f32_16x16x32_bf16 v[110:113], v[176:179], v[208:211], v[110:113]
	v_mfma_f32_16x16x32_bf16 v[102:105], v[168:171], v[220:223], v[102:105]
	v_mfma_f32_16x16x32_bf16 v[94:97], v[176:179], v[220:223], v[94:97]
	v_mfma_f32_16x16x32_bf16 v[86:89], v[168:171], v[228:231], v[86:89]
	v_mfma_f32_16x16x32_bf16 v[78:81], v[176:179], v[228:231], v[78:81]
	v_mfma_f32_16x16x32_bf16 v[126:129], v[172:175], v[204:207], v[126:129]
	v_mfma_f32_16x16x32_bf16 v[122:125], v[180:183], v[204:207], v[122:125]
	v_mfma_f32_16x16x32_bf16 v[118:121], v[172:175], v[216:219], v[118:121]
	v_mfma_f32_16x16x32_bf16 v[110:113], v[180:183], v[216:219], v[110:113]
	v_mfma_f32_16x16x32_bf16 v[102:105], v[172:175], v[224:227], v[102:105]
	v_mfma_f32_16x16x32_bf16 v[94:97], v[180:183], v[224:227], v[94:97]
	v_mfma_f32_16x16x32_bf16 v[86:89], v[172:175], v[232:235], v[86:89]
	v_mfma_f32_16x16x32_bf16 v[78:81], v[180:183], v[232:235], v[78:81]
	v_mfma_f32_16x16x32_bf16 v[114:117], v[184:187], v[200:203], v[114:117]
	v_mfma_f32_16x16x32_bf16 v[106:109], v[192:195], v[200:203], v[106:109]
	v_mfma_f32_16x16x32_bf16 v[98:101], v[184:187], v[208:211], v[98:101]
	v_mfma_f32_16x16x32_bf16 v[90:93], v[192:195], v[208:211], v[90:93]
	v_mfma_f32_16x16x32_bf16 v[82:85], v[184:187], v[220:223], v[82:85]
	v_mfma_f32_16x16x32_bf16 v[74:77], v[192:195], v[220:223], v[74:77]
	v_mfma_f32_16x16x32_bf16 v[70:73], v[184:187], v[228:231], v[70:73]
	v_mfma_f32_16x16x32_bf16 v[66:69], v[192:195], v[228:231], v[66:69]
	v_mfma_f32_16x16x32_bf16 v[114:117], v[188:191], v[204:207], v[114:117]
	v_mfma_f32_16x16x32_bf16 v[106:109], v[196:199], v[204:207], v[106:109]
	v_mfma_f32_16x16x32_bf16 v[98:101], v[188:191], v[216:219], v[98:101]
	v_mfma_f32_16x16x32_bf16 v[90:93], v[196:199], v[216:219], v[90:93]
	v_mfma_f32_16x16x32_bf16 v[82:85], v[188:191], v[224:227], v[82:85]
	v_mfma_f32_16x16x32_bf16 v[74:77], v[196:199], v[224:227], v[74:77]
	v_mfma_f32_16x16x32_bf16 v[70:73], v[188:191], v[232:235], v[70:73]
	v_mfma_f32_16x16x32_bf16 v[66:69], v[196:199], v[232:235], v[66:69]
	s_setprio 0
	s_barrier
	s_add_i32 s53, s48, s38
	v_lshl_add_u64 v[214:215], s[34:35], 0, v[130:131]
	s_mov_b32 m0, s53
	ds_read_b128 v[200:203], v161 offset:16384
	ds_read_b128 v[204:207], v161 offset:17408
	ds_read_b128 v[208:211], v161 offset:18432
	ds_read_b128 v[216:219], v161 offset:19456
	ds_read_b128 v[220:223], v161 offset:20480
	ds_read_b128 v[224:227], v161 offset:21504
	ds_read_b128 v[228:231], v161 offset:22528
	ds_read_b128 v[232:235], v161 offset:23552
	global_load_lds_dwordx4 v[214:215], off
	s_add_i32 m0, s53, 0x2000
	s_add_u32 s54, s34, 0x80000
	v_lshl_add_u64 v[236:237], s[34:35], 0, v[132:133]
	s_addc_u32 s55, s35, 0
	s_add_i32 s53, s49, s38
	global_load_lds_dwordx4 v[236:237], off
	v_lshl_add_u64 v[238:239], s[54:55], 0, v[130:131]
	s_mov_b32 m0, s53
	v_mov_b32_e32 v213, v135
	global_load_lds_dwordx4 v[238:239], off
	v_lshl_add_u64 v[238:239], s[54:55], 0, v[132:133]
	s_add_i32 m0, s53, 0x2000
	s_nop 0
	global_load_lds_dwordx4 v[238:239], off
	s_mov_b32 m0, s39
	v_lshl_add_u64 v[238:239], s[36:37], 0, v[134:135]
	global_load_lds_dwordx4 v134, s[36:37]
	s_mov_b32 m0, s40
	s_nop 0
	global_load_lds_dwordx4 v212, s[36:37]
	s_waitcnt vmcnt(8)
	s_waitcnt lgkmcnt(0)
	v_lshl_add_u64 v[212:213], s[36:37], 0, v[212:213]
	s_barrier
	s_setprio 1
	s_waitcnt lgkmcnt(0)
	v_mfma_f32_16x16x32_bf16 v[62:65], v[168:171], v[200:203], v[62:65]
	v_mfma_f32_16x16x32_bf16 v[58:61], v[176:179], v[200:203], v[58:61]
	v_mfma_f32_16x16x32_bf16 v[46:49], v[168:171], v[208:211], v[46:49]
	v_mfma_f32_16x16x32_bf16 v[30:33], v[176:179], v[208:211], v[30:33]
	v_mfma_f32_16x16x32_bf16 v[22:25], v[168:171], v[220:223], v[22:25]
	v_mfma_f32_16x16x32_bf16 v[14:17], v[176:179], v[220:223], v[14:17]
	v_mfma_f32_16x16x32_bf16 v[6:9], v[168:171], v[228:231], v[6:9]
	v_mfma_f32_16x16x32_bf16 v[2:5], v[176:179], v[228:231], v[2:5]
	v_mfma_f32_16x16x32_bf16 v[62:65], v[172:175], v[204:207], v[62:65]
	v_mfma_f32_16x16x32_bf16 v[58:61], v[180:183], v[204:207], v[58:61]
	v_mfma_f32_16x16x32_bf16 v[46:49], v[172:175], v[216:219], v[46:49]
	v_mfma_f32_16x16x32_bf16 v[30:33], v[180:183], v[216:219], v[30:33]
	v_mfma_f32_16x16x32_bf16 v[22:25], v[172:175], v[224:227], v[22:25]
	v_mfma_f32_16x16x32_bf16 v[14:17], v[180:183], v[224:227], v[14:17]
	v_mfma_f32_16x16x32_bf16 v[6:9], v[172:175], v[232:235], v[6:9]
	v_mfma_f32_16x16x32_bf16 v[2:5], v[180:183], v[232:235], v[2:5]
	v_mfma_f32_16x16x32_bf16 v[34:37], v[184:187], v[200:203], v[34:37]
	v_mfma_f32_16x16x32_bf16 v[26:29], v[192:195], v[200:203], v[26:29]
	v_mfma_f32_16x16x32_bf16 v[18:21], v[184:187], v[208:211], v[18:21]
	v_mfma_f32_16x16x32_bf16 v[10:13], v[192:195], v[208:211], v[10:13]
	v_mfma_f32_16x16x32_bf16 v[54:57], v[184:187], v[220:223], v[54:57]
	v_mfma_f32_16x16x32_bf16 v[50:53], v[192:195], v[220:223], v[50:53]
	v_mfma_f32_16x16x32_bf16 v[42:45], v[184:187], v[228:231], v[42:45]
	v_mfma_f32_16x16x32_bf16 v[38:41], v[192:195], v[228:231], v[38:41]
	v_mfma_f32_16x16x32_bf16 v[34:37], v[188:191], v[204:207], v[34:37]
	v_mfma_f32_16x16x32_bf16 v[26:29], v[196:199], v[204:207], v[26:29]
	v_mfma_f32_16x16x32_bf16 v[18:21], v[188:191], v[216:219], v[18:21]
	v_mfma_f32_16x16x32_bf16 v[10:13], v[196:199], v[216:219], v[10:13]
	v_mfma_f32_16x16x32_bf16 v[54:57], v[188:191], v[224:227], v[54:57]
	v_mfma_f32_16x16x32_bf16 v[50:53], v[196:199], v[224:227], v[50:53]
	v_mfma_f32_16x16x32_bf16 v[42:45], v[188:191], v[232:235], v[42:45]
	v_mfma_f32_16x16x32_bf16 v[38:41], v[196:199], v[232:235], v[38:41]
	s_setprio 0
	s_barrier
	s_add_i32 s53, 0, 0x18000
	v_add_u32_e32 v134, s53, v158
	s_add_i32 s54, 0, 0x1c000
	ds_read_b128 v[168:171], v134
	ds_read_b128 v[172:175], v134 offset:1024
	ds_read_b128 v[176:179], v134 offset:2048
	ds_read_b128 v[180:183], v134 offset:3072
	v_add_u32_e32 v134, s54, v158
	ds_read_b128 v[184:187], v134
	ds_read_b128 v[188:191], v134 offset:1024
	ds_read_b128 v[192:195], v134 offset:2048
	ds_read_b128 v[196:199], v134 offset:3072
	s_mov_b32 m0, s41
	ds_read_b128 v[200:203], v161 offset:32768
	ds_read_b128 v[204:207], v161 offset:33792
	ds_read_b128 v[208:211], v161 offset:34816
	ds_read_b128 v[216:219], v161 offset:35840
	ds_read_b128 v[220:223], v161 offset:36864
	ds_read_b128 v[224:227], v161 offset:37888
	ds_read_b128 v[228:231], v161 offset:38912
	ds_read_b128 v[232:235], v161 offset:39936
	global_load_lds_dwordx4 v145, s[36:37]
	s_mov_b32 m0, s42
	s_nop 0
	global_load_lds_dwordx4 v147, s[36:37]
	s_waitcnt vmcnt(8)
	s_waitcnt lgkmcnt(0)
	s_barrier
	s_setprio 1
	s_waitcnt lgkmcnt(0)
	v_mfma_f32_16x16x32_bf16 v[126:129], v[168:171], v[200:203], v[126:129]
	v_mfma_f32_16x16x32_bf16 v[122:125], v[176:179], v[200:203], v[122:125]
	v_mfma_f32_16x16x32_bf16 v[118:121], v[168:171], v[208:211], v[118:121]
	v_mfma_f32_16x16x32_bf16 v[110:113], v[176:179], v[208:211], v[110:113]
	v_mfma_f32_16x16x32_bf16 v[102:105], v[168:171], v[220:223], v[102:105]
	v_mfma_f32_16x16x32_bf16 v[94:97], v[176:179], v[220:223], v[94:97]
	v_mfma_f32_16x16x32_bf16 v[86:89], v[168:171], v[228:231], v[86:89]
	v_mfma_f32_16x16x32_bf16 v[78:81], v[176:179], v[228:231], v[78:81]
	v_mfma_f32_16x16x32_bf16 v[126:129], v[172:175], v[204:207], v[126:129]
	v_mfma_f32_16x16x32_bf16 v[122:125], v[180:183], v[204:207], v[122:125]
	v_mfma_f32_16x16x32_bf16 v[118:121], v[172:175], v[216:219], v[118:121]
	v_mfma_f32_16x16x32_bf16 v[110:113], v[180:183], v[216:219], v[110:113]
	v_mfma_f32_16x16x32_bf16 v[102:105], v[172:175], v[224:227], v[102:105]
	v_mfma_f32_16x16x32_bf16 v[94:97], v[180:183], v[224:227], v[94:97]
	v_mfma_f32_16x16x32_bf16 v[86:89], v[172:175], v[232:235], v[86:89]
	v_mfma_f32_16x16x32_bf16 v[78:81], v[180:183], v[232:235], v[78:81]
	v_mfma_f32_16x16x32_bf16 v[114:117], v[184:187], v[200:203], v[114:117]
	v_mfma_f32_16x16x32_bf16 v[106:109], v[192:195], v[200:203], v[106:109]
	v_mfma_f32_16x16x32_bf16 v[98:101], v[184:187], v[208:211], v[98:101]
	v_mfma_f32_16x16x32_bf16 v[90:93], v[192:195], v[208:211], v[90:93]
	v_mfma_f32_16x16x32_bf16 v[82:85], v[184:187], v[220:223], v[82:85]
	v_mfma_f32_16x16x32_bf16 v[74:77], v[192:195], v[220:223], v[74:77]
	v_mfma_f32_16x16x32_bf16 v[70:73], v[184:187], v[228:231], v[70:73]
	v_mfma_f32_16x16x32_bf16 v[66:69], v[192:195], v[228:231], v[66:69]
	v_mfma_f32_16x16x32_bf16 v[114:117], v[188:191], v[204:207], v[114:117]
	v_mfma_f32_16x16x32_bf16 v[106:109], v[196:199], v[204:207], v[106:109]
	v_mfma_f32_16x16x32_bf16 v[98:101], v[188:191], v[216:219], v[98:101]
	v_mfma_f32_16x16x32_bf16 v[90:93], v[196:199], v[216:219], v[90:93]
	v_mfma_f32_16x16x32_bf16 v[82:85], v[188:191], v[224:227], v[82:85]
	v_mfma_f32_16x16x32_bf16 v[74:77], v[196:199], v[224:227], v[74:77]
	v_mfma_f32_16x16x32_bf16 v[70:73], v[188:191], v[232:235], v[70:73]
	v_mfma_f32_16x16x32_bf16 v[66:69], v[196:199], v[232:235], v[66:69]
	s_setprio 0
	s_barrier
	s_add_i32 s36, s53, s38
	v_lshl_add_u64 v[214:215], v[214:215], 0, s[16:17]
	s_mov_b32 m0, s36
	ds_read_b128 v[200:203], v161 offset:49152
	ds_read_b128 v[204:207], v161 offset:50176
	ds_read_b128 v[208:211], v161 offset:51200
	ds_read_b128 v[216:219], v161 offset:52224
	ds_read_b128 v[220:223], v161 offset:53248
	ds_read_b128 v[224:227], v161 offset:54272
	ds_read_b128 v[228:231], v161 offset:55296
	ds_read_b128 v[232:235], v161 offset:56320
	global_load_lds_dwordx4 v[214:215], off
	s_add_i32 m0, s36, 0x2000
	s_add_u32 s34, s34, 0x80080
	v_lshl_add_u64 v[214:215], v[236:237], 0, s[16:17]
	s_addc_u32 s35, s35, 0
	s_add_i32 s36, s54, s38
	global_load_lds_dwordx4 v[214:215], off
	v_lshl_add_u64 v[214:215], s[34:35], 0, v[130:131]
	s_mov_b32 m0, s36
	v_lshl_add_u64 v[212:213], v[212:213], 0, s[16:17]
	global_load_lds_dwordx4 v[214:215], off
	v_lshl_add_u64 v[214:215], s[34:35], 0, v[132:133]
	s_add_i32 m0, s36, 0x2000
	s_nop 0
	global_load_lds_dwordx4 v[214:215], off
	v_lshl_add_u64 v[214:215], v[238:239], 0, s[16:17]
	s_mov_b32 m0, s43
	s_nop 0
	global_load_lds_dwordx4 v[214:215], off
	s_mov_b32 m0, s44
	s_nop 0
	global_load_lds_dwordx4 v[212:213], off
	s_waitcnt vmcnt(8)
	s_waitcnt lgkmcnt(0)
	s_barrier
	s_setprio 1
	s_waitcnt lgkmcnt(0)
	v_mfma_f32_16x16x32_bf16 v[62:65], v[168:171], v[200:203], v[62:65]
	v_mfma_f32_16x16x32_bf16 v[58:61], v[176:179], v[200:203], v[58:61]
	v_mfma_f32_16x16x32_bf16 v[46:49], v[168:171], v[208:211], v[46:49]
	v_mfma_f32_16x16x32_bf16 v[30:33], v[176:179], v[208:211], v[30:33]
	v_mfma_f32_16x16x32_bf16 v[22:25], v[168:171], v[220:223], v[22:25]
	v_mfma_f32_16x16x32_bf16 v[14:17], v[176:179], v[220:223], v[14:17]
	v_mfma_f32_16x16x32_bf16 v[6:9], v[168:171], v[228:231], v[6:9]
	v_mfma_f32_16x16x32_bf16 v[2:5], v[176:179], v[228:231], v[2:5]
	v_mfma_f32_16x16x32_bf16 v[62:65], v[172:175], v[204:207], v[62:65]
	v_mfma_f32_16x16x32_bf16 v[58:61], v[180:183], v[204:207], v[58:61]
	v_mfma_f32_16x16x32_bf16 v[46:49], v[172:175], v[216:219], v[46:49]
	v_mfma_f32_16x16x32_bf16 v[30:33], v[180:183], v[216:219], v[30:33]
	v_mfma_f32_16x16x32_bf16 v[22:25], v[172:175], v[224:227], v[22:25]
	v_mfma_f32_16x16x32_bf16 v[14:17], v[180:183], v[224:227], v[14:17]
	v_mfma_f32_16x16x32_bf16 v[6:9], v[172:175], v[232:235], v[6:9]
	v_mfma_f32_16x16x32_bf16 v[2:5], v[180:183], v[232:235], v[2:5]
	v_mfma_f32_16x16x32_bf16 v[34:37], v[184:187], v[200:203], v[34:37]
	v_mfma_f32_16x16x32_bf16 v[26:29], v[192:195], v[200:203], v[26:29]
	v_mfma_f32_16x16x32_bf16 v[18:21], v[184:187], v[208:211], v[18:21]
	v_mfma_f32_16x16x32_bf16 v[10:13], v[192:195], v[208:211], v[10:13]
	v_mfma_f32_16x16x32_bf16 v[54:57], v[184:187], v[220:223], v[54:57]
	v_mfma_f32_16x16x32_bf16 v[50:53], v[192:195], v[220:223], v[50:53]
	v_mfma_f32_16x16x32_bf16 v[42:45], v[184:187], v[228:231], v[42:45]
	v_mfma_f32_16x16x32_bf16 v[38:41], v[192:195], v[228:231], v[38:41]
	v_mfma_f32_16x16x32_bf16 v[34:37], v[188:191], v[204:207], v[34:37]
	v_mfma_f32_16x16x32_bf16 v[26:29], v[196:199], v[204:207], v[26:29]
	v_mfma_f32_16x16x32_bf16 v[18:21], v[188:191], v[216:219], v[18:21]
	v_mfma_f32_16x16x32_bf16 v[10:13], v[196:199], v[216:219], v[10:13]
	v_mfma_f32_16x16x32_bf16 v[54:57], v[188:191], v[224:227], v[54:57]
	v_mfma_f32_16x16x32_bf16 v[50:53], v[196:199], v[224:227], v[50:53]
	v_mfma_f32_16x16x32_bf16 v[42:45], v[188:191], v[232:235], v[42:45]
	v_mfma_f32_16x16x32_bf16 v[38:41], v[196:199], v[232:235], v[38:41]
	s_setprio 0
	s_barrier
	s_add_i32 s52, s52, 2
	s_add_u32 s30, s30, 0x100
	s_addc_u32 s31, s31, 0
	s_cmp_gt_u32 s52, 29
	s_cbranch_scc0 .LBB0_386
	s_and_b64 vcc, exec, s[20:21]
	s_cbranch_vccz .LBB0_399
	s_barrier
	s_cmp_gt_i32 s28, 23
	s_mov_b64 s[30:31], -1
	s_cbranch_scc1 .LBB0_400

.LBB0_892:
	ds_read_b128 v[168:171], v160
	ds_read_b128 v[172:175], v160 offset:1024
	ds_read_b128 v[176:179], v160 offset:2048
	ds_read_b128 v[180:183], v160 offset:3072
	ds_read_b128 v[184:187], v161
	ds_read_b128 v[188:191], v161 offset:1024
	ds_read_b128 v[192:195], v161 offset:2048
	ds_read_b128 v[196:199], v161 offset:3072
	s_add_u32 s34, s84, s30
	s_addc_u32 s35, s85, s31
	s_add_u32 s36, s34, 0x25300100
	s_addc_u32 s37, s35, 0
	s_add_u32 s70, s29, s30
	s_addc_u32 s71, s58, s31
	s_cmpk_eq_i32 s30, 0xf00
	s_cselect_b64 vcc, -1, 0
	s_and_b64 s[34:35], vcc, exec
	v_cndmask_b32_e32 v136, v143, v163, vcc
	s_cselect_b32 s37, s9, s37
	s_cselect_b32 s36, s8, s36
	v_cndmask_b32_e32 v145, v144, v164, vcc
	v_cndmask_b32_e32 v232, v142, v165, vcc
	v_cndmask_b32_e32 v147, v146, v166, vcc
	s_cselect_b32 s35, s7, s71
	s_cselect_b32 s34, s6, s70
	v_lshl_add_u64 v[234:235], v[150:151], 0, s[30:31]
	s_add_i32 m0, s40, 0xc000
	ds_read_b128 v[200:203], v162
	ds_read_b128 v[204:207], v162 offset:1024
	ds_read_b128 v[208:211], v162 offset:2048
	ds_read_b128 v[212:215], v162 offset:3072
	ds_read_b128 v[216:219], v162 offset:4096
	ds_read_b128 v[220:223], v162 offset:5120
	ds_read_b128 v[224:227], v162 offset:6144
	ds_read_b128 v[228:231], v162 offset:7168
	global_load_lds_dwordx4 v[234:235], off
	v_lshl_add_u64 v[234:235], v[148:149], 0, s[30:31]
	s_add_i32 m0, s40, 0xe000
	s_nop 0
	global_load_lds_dwordx4 v[234:235], off
	s_waitcnt vmcnt(8)
	s_waitcnt lgkmcnt(0)
	s_barrier
	s_setprio 1
	s_waitcnt lgkmcnt(0)
	v_mfma_f32_16x16x32_bf16 v[126:129], v[168:171], v[200:203], v[126:129]
	v_mfma_f32_16x16x32_bf16 v[122:125], v[176:179], v[200:203], v[122:125]
	v_mfma_f32_16x16x32_bf16 v[118:121], v[168:171], v[208:211], v[118:121]
	v_mfma_f32_16x16x32_bf16 v[110:113], v[176:179], v[208:211], v[110:113]
	v_mfma_f32_16x16x32_bf16 v[102:105], v[168:171], v[216:219], v[102:105]
	v_mfma_f32_16x16x32_bf16 v[94:97], v[176:179], v[216:219], v[94:97]
	v_mfma_f32_16x16x32_bf16 v[86:89], v[168:171], v[224:227], v[86:89]
	v_mfma_f32_16x16x32_bf16 v[78:81], v[176:179], v[224:227], v[78:81]
	v_mfma_f32_16x16x32_bf16 v[126:129], v[172:175], v[204:207], v[126:129]
	v_mfma_f32_16x16x32_bf16 v[122:125], v[180:183], v[204:207], v[122:125]
	v_mfma_f32_16x16x32_bf16 v[118:121], v[172:175], v[212:215], v[118:121]
	v_mfma_f32_16x16x32_bf16 v[110:113], v[180:183], v[212:215], v[110:113]
	v_mfma_f32_16x16x32_bf16 v[102:105], v[172:175], v[220:223], v[102:105]
	v_mfma_f32_16x16x32_bf16 v[94:97], v[180:183], v[220:223], v[94:97]
	v_mfma_f32_16x16x32_bf16 v[86:89], v[172:175], v[228:231], v[86:89]
	v_mfma_f32_16x16x32_bf16 v[78:81], v[180:183], v[228:231], v[78:81]
	v_mfma_f32_16x16x32_bf16 v[114:117], v[184:187], v[200:203], v[114:117]
	v_mfma_f32_16x16x32_bf16 v[106:109], v[192:195], v[200:203], v[106:109]
	v_mfma_f32_16x16x32_bf16 v[98:101], v[184:187], v[208:211], v[98:101]
	v_mfma_f32_16x16x32_bf16 v[90:93], v[192:195], v[208:211], v[90:93]
	v_mfma_f32_16x16x32_bf16 v[82:85], v[184:187], v[216:219], v[82:85]
	v_mfma_f32_16x16x32_bf16 v[74:77], v[192:195], v[216:219], v[74:77]
	v_mfma_f32_16x16x32_bf16 v[70:73], v[184:187], v[224:227], v[70:73]
	v_mfma_f32_16x16x32_bf16 v[66:69], v[192:195], v[224:227], v[66:69]
	v_mfma_f32_16x16x32_bf16 v[114:117], v[188:191], v[204:207], v[114:117]
	v_mfma_f32_16x16x32_bf16 v[106:109], v[196:199], v[204:207], v[106:109]
	v_mfma_f32_16x16x32_bf16 v[98:101], v[188:191], v[212:215], v[98:101]
	v_mfma_f32_16x16x32_bf16 v[90:93], v[196:199], v[212:215], v[90:93]
	v_mfma_f32_16x16x32_bf16 v[82:85], v[188:191], v[220:223], v[82:85]
	v_mfma_f32_16x16x32_bf16 v[74:77], v[196:199], v[220:223], v[74:77]
	v_mfma_f32_16x16x32_bf16 v[70:73], v[188:191], v[228:231], v[70:73]
	v_mfma_f32_16x16x32_bf16 v[66:69], v[196:199], v[228:231], v[66:69]
	s_setprio 0
	s_barrier
	s_add_i32 s70, s49, s39
	v_lshl_add_u64 v[234:235], s[34:35], 0, v[132:133]
	s_mov_b32 m0, s70
	ds_read_b128 v[200:203], v162 offset:16384
	ds_read_b128 v[204:207], v162 offset:17408
	ds_read_b128 v[208:211], v162 offset:18432
	ds_read_b128 v[212:215], v162 offset:19456
	ds_read_b128 v[216:219], v162 offset:20480
	ds_read_b128 v[220:223], v162 offset:21504
	ds_read_b128 v[224:227], v162 offset:22528
	ds_read_b128 v[228:231], v162 offset:23552
	global_load_lds_dwordx4 v[234:235], off
	s_add_i32 m0, s70, 0x2000
	s_add_u32 s70, s34, 0x80000
	v_lshl_add_u64 v[236:237], s[34:35], 0, v[134:135]
	s_addc_u32 s71, s35, 0
	s_add_i32 s74, s50, s39
	global_load_lds_dwordx4 v[236:237], off
	v_lshl_add_u64 v[238:239], s[70:71], 0, v[132:133]
	s_mov_b32 m0, s74
	v_mov_b32_e32 v233, v137
	global_load_lds_dwordx4 v[238:239], off
	v_lshl_add_u64 v[238:239], s[70:71], 0, v[134:135]
	s_add_i32 m0, s74, 0x2000
	s_nop 0
	global_load_lds_dwordx4 v[238:239], off
	s_mov_b32 m0, s40
	v_lshl_add_u64 v[238:239], s[36:37], 0, v[136:137]
	global_load_lds_dwordx4 v136, s[36:37]
	s_mov_b32 m0, s41
	s_nop 0
	global_load_lds_dwordx4 v232, s[36:37]
	s_waitcnt vmcnt(8)
	s_waitcnt lgkmcnt(0)
	v_lshl_add_u64 v[232:233], s[36:37], 0, v[232:233]
	s_barrier
	s_setprio 1
	s_waitcnt lgkmcnt(0)
	v_mfma_f32_16x16x32_bf16 v[62:65], v[168:171], v[200:203], v[62:65]
	v_mfma_f32_16x16x32_bf16 v[58:61], v[176:179], v[200:203], v[58:61]
	v_mfma_f32_16x16x32_bf16 v[46:49], v[168:171], v[208:211], v[46:49]
	v_mfma_f32_16x16x32_bf16 v[38:41], v[176:179], v[208:211], v[38:41]
	v_mfma_f32_16x16x32_bf16 v[22:25], v[168:171], v[216:219], v[22:25]
	v_mfma_f32_16x16x32_bf16 v[14:17], v[176:179], v[216:219], v[14:17]
	v_mfma_f32_16x16x32_bf16 v[6:9], v[168:171], v[224:227], v[6:9]
	v_mfma_f32_16x16x32_bf16 v[2:5], v[176:179], v[224:227], v[2:5]
	v_mfma_f32_16x16x32_bf16 v[62:65], v[172:175], v[204:207], v[62:65]
	v_mfma_f32_16x16x32_bf16 v[58:61], v[180:183], v[204:207], v[58:61]
	v_mfma_f32_16x16x32_bf16 v[46:49], v[172:175], v[212:215], v[46:49]
	v_mfma_f32_16x16x32_bf16 v[38:41], v[180:183], v[212:215], v[38:41]
	v_mfma_f32_16x16x32_bf16 v[22:25], v[172:175], v[220:223], v[22:25]
	v_mfma_f32_16x16x32_bf16 v[14:17], v[180:183], v[220:223], v[14:17]
	v_mfma_f32_16x16x32_bf16 v[6:9], v[172:175], v[228:231], v[6:9]
	v_mfma_f32_16x16x32_bf16 v[2:5], v[180:183], v[228:231], v[2:5]
	v_mfma_f32_16x16x32_bf16 v[42:45], v[184:187], v[200:203], v[42:45]
	v_mfma_f32_16x16x32_bf16 v[30:33], v[192:195], v[200:203], v[30:33]
	v_mfma_f32_16x16x32_bf16 v[18:21], v[184:187], v[208:211], v[18:21]
	v_mfma_f32_16x16x32_bf16 v[10:13], v[192:195], v[208:211], v[10:13]
	v_mfma_f32_16x16x32_bf16 v[54:57], v[184:187], v[216:219], v[54:57]
	v_mfma_f32_16x16x32_bf16 v[50:53], v[192:195], v[216:219], v[50:53]
	v_mfma_f32_16x16x32_bf16 v[34:37], v[184:187], v[224:227], v[34:37]
	v_mfma_f32_16x16x32_bf16 v[26:29], v[192:195], v[224:227], v[26:29]
	v_mfma_f32_16x16x32_bf16 v[42:45], v[188:191], v[204:207], v[42:45]
	v_mfma_f32_16x16x32_bf16 v[30:33], v[196:199], v[204:207], v[30:33]
	v_mfma_f32_16x16x32_bf16 v[18:21], v[188:191], v[212:215], v[18:21]
	v_mfma_f32_16x16x32_bf16 v[10:13], v[196:199], v[212:215], v[10:13]
	v_mfma_f32_16x16x32_bf16 v[54:57], v[188:191], v[220:223], v[54:57]
	v_mfma_f32_16x16x32_bf16 v[50:53], v[196:199], v[220:223], v[50:53]
	v_mfma_f32_16x16x32_bf16 v[34:37], v[188:191], v[228:231], v[34:37]
	v_mfma_f32_16x16x32_bf16 v[26:29], v[196:199], v[228:231], v[26:29]
	s_setprio 0
	s_barrier
	s_add_i32 s70, 0, 0x18000
	v_add_u32_e32 v136, s70, v158
	s_add_i32 s71, 0, 0x1c000
	ds_read_b128 v[168:171], v136
	ds_read_b128 v[172:175], v136 offset:1024
	ds_read_b128 v[176:179], v136 offset:2048
	ds_read_b128 v[180:183], v136 offset:3072
	v_add_u32_e32 v136, s71, v158
	ds_read_b128 v[184:187], v136
	ds_read_b128 v[188:191], v136 offset:1024
	ds_read_b128 v[192:195], v136 offset:2048
	ds_read_b128 v[196:199], v136 offset:3072
	s_mov_b32 m0, s42
	ds_read_b128 v[200:203], v162 offset:32768
	ds_read_b128 v[204:207], v162 offset:33792
	ds_read_b128 v[208:211], v162 offset:34816
	ds_read_b128 v[212:215], v162 offset:35840
	ds_read_b128 v[216:219], v162 offset:36864
	ds_read_b128 v[220:223], v162 offset:37888
	ds_read_b128 v[224:227], v162 offset:38912
	ds_read_b128 v[228:231], v162 offset:39936
	global_load_lds_dwordx4 v145, s[36:37]
	s_mov_b32 m0, s43
	s_nop 0
	global_load_lds_dwordx4 v147, s[36:37]
	s_waitcnt vmcnt(8)
	s_waitcnt lgkmcnt(0)
	s_barrier
	s_setprio 1
	s_waitcnt lgkmcnt(0)
	v_mfma_f32_16x16x32_bf16 v[126:129], v[168:171], v[200:203], v[126:129]
	v_mfma_f32_16x16x32_bf16 v[122:125], v[176:179], v[200:203], v[122:125]
	v_mfma_f32_16x16x32_bf16 v[118:121], v[168:171], v[208:211], v[118:121]
	v_mfma_f32_16x16x32_bf16 v[110:113], v[176:179], v[208:211], v[110:113]
	v_mfma_f32_16x16x32_bf16 v[102:105], v[168:171], v[216:219], v[102:105]
	v_mfma_f32_16x16x32_bf16 v[94:97], v[176:179], v[216:219], v[94:97]
	v_mfma_f32_16x16x32_bf16 v[86:89], v[168:171], v[224:227], v[86:89]
	v_mfma_f32_16x16x32_bf16 v[78:81], v[176:179], v[224:227], v[78:81]
	v_mfma_f32_16x16x32_bf16 v[126:129], v[172:175], v[204:207], v[126:129]
	v_mfma_f32_16x16x32_bf16 v[122:125], v[180:183], v[204:207], v[122:125]
	v_mfma_f32_16x16x32_bf16 v[118:121], v[172:175], v[212:215], v[118:121]
	v_mfma_f32_16x16x32_bf16 v[110:113], v[180:183], v[212:215], v[110:113]
	v_mfma_f32_16x16x32_bf16 v[102:105], v[172:175], v[220:223], v[102:105]
	v_mfma_f32_16x16x32_bf16 v[94:97], v[180:183], v[220:223], v[94:97]
	v_mfma_f32_16x16x32_bf16 v[86:89], v[172:175], v[228:231], v[86:89]
	v_mfma_f32_16x16x32_bf16 v[78:81], v[180:183], v[228:231], v[78:81]
	v_mfma_f32_16x16x32_bf16 v[114:117], v[184:187], v[200:203], v[114:117]
	v_mfma_f32_16x16x32_bf16 v[106:109], v[192:195], v[200:203], v[106:109]
	v_mfma_f32_16x16x32_bf16 v[98:101], v[184:187], v[208:211], v[98:101]
	v_mfma_f32_16x16x32_bf16 v[90:93], v[192:195], v[208:211], v[90:93]
	v_mfma_f32_16x16x32_bf16 v[82:85], v[184:187], v[216:219], v[82:85]
	v_mfma_f32_16x16x32_bf16 v[74:77], v[192:195], v[216:219], v[74:77]
	v_mfma_f32_16x16x32_bf16 v[70:73], v[184:187], v[224:227], v[70:73]
	v_mfma_f32_16x16x32_bf16 v[66:69], v[192:195], v[224:227], v[66:69]
	v_mfma_f32_16x16x32_bf16 v[114:117], v[188:191], v[204:207], v[114:117]
	v_mfma_f32_16x16x32_bf16 v[106:109], v[196:199], v[204:207], v[106:109]
	v_mfma_f32_16x16x32_bf16 v[98:101], v[188:191], v[212:215], v[98:101]
	v_mfma_f32_16x16x32_bf16 v[90:93], v[196:199], v[212:215], v[90:93]
	v_mfma_f32_16x16x32_bf16 v[82:85], v[188:191], v[220:223], v[82:85]
	v_mfma_f32_16x16x32_bf16 v[74:77], v[196:199], v[220:223], v[74:77]
	v_mfma_f32_16x16x32_bf16 v[70:73], v[188:191], v[228:231], v[70:73]
	v_mfma_f32_16x16x32_bf16 v[66:69], v[196:199], v[228:231], v[66:69]
	s_setprio 0
	s_barrier
	s_add_i32 s36, s70, s39
	v_lshl_add_u64 v[234:235], v[234:235], 0, s[16:17]
	s_mov_b32 m0, s36
	ds_read_b128 v[200:203], v162 offset:49152
	ds_read_b128 v[204:207], v162 offset:50176
	ds_read_b128 v[208:211], v162 offset:51200
	ds_read_b128 v[212:215], v162 offset:52224
	ds_read_b128 v[216:219], v162 offset:53248
	ds_read_b128 v[220:223], v162 offset:54272
	ds_read_b128 v[224:227], v162 offset:55296
	ds_read_b128 v[228:231], v162 offset:56320
	global_load_lds_dwordx4 v[234:235], off
	s_add_i32 m0, s36, 0x2000
	s_add_u32 s34, s34, 0x80080
	v_lshl_add_u64 v[234:235], v[236:237], 0, s[16:17]
	s_addc_u32 s35, s35, 0
	s_add_i32 s36, s71, s39
	global_load_lds_dwordx4 v[234:235], off
	v_lshl_add_u64 v[234:235], s[34:35], 0, v[132:133]
	s_mov_b32 m0, s36
	v_lshl_add_u64 v[232:233], v[232:233], 0, s[16:17]
	global_load_lds_dwordx4 v[234:235], off
	v_lshl_add_u64 v[234:235], s[34:35], 0, v[134:135]
	s_add_i32 m0, s36, 0x2000
	s_nop 0
	global_load_lds_dwordx4 v[234:235], off
	v_lshl_add_u64 v[234:235], v[238:239], 0, s[16:17]
	s_mov_b32 m0, s45
	s_nop 0
	global_load_lds_dwordx4 v[234:235], off
	s_mov_b32 m0, s47
	s_nop 0
	global_load_lds_dwordx4 v[232:233], off
	s_waitcnt vmcnt(8)
	s_waitcnt lgkmcnt(0)
	s_barrier
	s_setprio 1
	s_waitcnt lgkmcnt(0)
	v_mfma_f32_16x16x32_bf16 v[62:65], v[168:171], v[200:203], v[62:65]
	v_mfma_f32_16x16x32_bf16 v[58:61], v[176:179], v[200:203], v[58:61]
	v_mfma_f32_16x16x32_bf16 v[46:49], v[168:171], v[208:211], v[46:49]
	v_mfma_f32_16x16x32_bf16 v[38:41], v[176:179], v[208:211], v[38:41]
	v_mfma_f32_16x16x32_bf16 v[22:25], v[168:171], v[216:219], v[22:25]
	v_mfma_f32_16x16x32_bf16 v[14:17], v[176:179], v[216:219], v[14:17]
	v_mfma_f32_16x16x32_bf16 v[6:9], v[168:171], v[224:227], v[6:9]
	v_mfma_f32_16x16x32_bf16 v[2:5], v[176:179], v[224:227], v[2:5]
	v_mfma_f32_16x16x32_bf16 v[62:65], v[172:175], v[204:207], v[62:65]
	v_mfma_f32_16x16x32_bf16 v[58:61], v[180:183], v[204:207], v[58:61]
	v_mfma_f32_16x16x32_bf16 v[46:49], v[172:175], v[212:215], v[46:49]
	v_mfma_f32_16x16x32_bf16 v[38:41], v[180:183], v[212:215], v[38:41]
	v_mfma_f32_16x16x32_bf16 v[22:25], v[172:175], v[220:223], v[22:25]
	v_mfma_f32_16x16x32_bf16 v[14:17], v[180:183], v[220:223], v[14:17]
	v_mfma_f32_16x16x32_bf16 v[6:9], v[172:175], v[228:231], v[6:9]
	v_mfma_f32_16x16x32_bf16 v[2:5], v[180:183], v[228:231], v[2:5]
	v_mfma_f32_16x16x32_bf16 v[42:45], v[184:187], v[200:203], v[42:45]
	v_mfma_f32_16x16x32_bf16 v[30:33], v[192:195], v[200:203], v[30:33]
	v_mfma_f32_16x16x32_bf16 v[18:21], v[184:187], v[208:211], v[18:21]
	v_mfma_f32_16x16x32_bf16 v[10:13], v[192:195], v[208:211], v[10:13]
	v_mfma_f32_16x16x32_bf16 v[54:57], v[184:187], v[216:219], v[54:57]
	v_mfma_f32_16x16x32_bf16 v[50:53], v[192:195], v[216:219], v[50:53]
	v_mfma_f32_16x16x32_bf16 v[34:37], v[184:187], v[224:227], v[34:37]
	v_mfma_f32_16x16x32_bf16 v[26:29], v[192:195], v[224:227], v[26:29]
	v_mfma_f32_16x16x32_bf16 v[42:45], v[188:191], v[204:207], v[42:45]
	v_mfma_f32_16x16x32_bf16 v[30:33], v[196:199], v[204:207], v[30:33]
	v_mfma_f32_16x16x32_bf16 v[18:21], v[188:191], v[212:215], v[18:21]
	v_mfma_f32_16x16x32_bf16 v[10:13], v[196:199], v[212:215], v[10:13]
	v_mfma_f32_16x16x32_bf16 v[54:57], v[188:191], v[220:223], v[54:57]
	v_mfma_f32_16x16x32_bf16 v[50:53], v[196:199], v[220:223], v[50:53]
	v_mfma_f32_16x16x32_bf16 v[34:37], v[188:191], v[228:231], v[34:37]
	v_mfma_f32_16x16x32_bf16 v[26:29], v[196:199], v[228:231], v[26:29]
	s_setprio 0
	s_barrier
	s_add_i32 s59, s59, 2
	s_add_u32 s30, s30, 0x100
	s_addc_u32 s31, s31, 0
	s_cmp_gt_u32 s59, 29
	s_cbranch_scc0 .LBB0_892
	s_and_b64 vcc, exec, s[20:21]
	s_cbranch_vccz .LBB0_895
	s_barrier

.LBB0_1065:
	v_add_u32_e32 v180, s56, v162
	v_add_u32_e32 v196, s57, v162
	s_add_u32 s30, s84, s6
	ds_read_b128 v[168:171], v180
	ds_read_b128 v[172:175], v180 offset:1024
	ds_read_b128 v[176:179], v180 offset:2048
	ds_read_b128 v[180:183], v180 offset:3072
	ds_read_b128 v[184:187], v196
	ds_read_b128 v[188:191], v196 offset:1024
	ds_read_b128 v[192:195], v196 offset:2048
	ds_read_b128 v[196:199], v196 offset:3072
	s_addc_u32 s31, s85, s7
	s_add_u32 s75, s30, 0x25300100
	s_addc_u32 s76, s31, 0
	s_cmpk_eq_i32 s6, 0xf00
	s_cselect_b64 vcc, -1, 0
	v_lshl_add_u64 v[156:157], v[154:155], 0, s[6:7]
	s_and_b64 s[30:31], vcc, exec
	s_cselect_b32 s31, s11, s76
	s_cselect_b32 s30, s10, s75
	v_cndmask_b32_e32 v136, v147, v139, vcc
	v_cndmask_b32_e32 v145, v144, v165, vcc
	v_cndmask_b32_e32 v212, v146, v166, vcc
	v_cndmask_b32_e32 v149, v148, v167, vcc
	v_cndmask_b32_e32 v157, v157, v143, vcc
	v_cndmask_b32_e32 v156, v156, v142, vcc
	s_mov_b32 m0, s69
	v_lshl_add_u64 v[236:237], v[152:153], 0, s[6:7]
	ds_read_b128 v[200:203], v164
	ds_read_b128 v[204:207], v164 offset:1024
	ds_read_b128 v[208:211], v164 offset:2048
	ds_read_b128 v[216:219], v164 offset:3072
	ds_read_b128 v[220:223], v164 offset:4096
	ds_read_b128 v[224:227], v164 offset:5120
	ds_read_b128 v[228:231], v164 offset:6144
	ds_read_b128 v[232:235], v164 offset:7168
	global_load_lds_dwordx4 v[236:237], off
	v_lshl_add_u64 v[236:237], v[150:151], 0, s[6:7]
	s_mov_b32 m0, s70
	s_nop 0
	global_load_lds_dwordx4 v[236:237], off
	s_waitcnt vmcnt(8)
	s_waitcnt lgkmcnt(0)
	s_barrier
	s_setprio 1
	s_waitcnt lgkmcnt(0)
	v_mfma_f32_16x16x32_bf16 v[126:129], v[168:171], v[200:203], v[126:129]
	v_mfma_f32_16x16x32_bf16 v[118:121], v[176:179], v[200:203], v[118:121]
	v_mfma_f32_16x16x32_bf16 v[110:113], v[168:171], v[208:211], v[110:113]
	v_mfma_f32_16x16x32_bf16 v[102:105], v[176:179], v[208:211], v[102:105]
	v_mfma_f32_16x16x32_bf16 v[94:97], v[168:171], v[220:223], v[94:97]
	v_mfma_f32_16x16x32_bf16 v[86:89], v[176:179], v[220:223], v[86:89]
	v_mfma_f32_16x16x32_bf16 v[78:81], v[168:171], v[228:231], v[78:81]
	v_mfma_f32_16x16x32_bf16 v[70:73], v[176:179], v[228:231], v[70:73]
	v_mfma_f32_16x16x32_bf16 v[126:129], v[172:175], v[204:207], v[126:129]
	v_mfma_f32_16x16x32_bf16 v[118:121], v[180:183], v[204:207], v[118:121]
	v_mfma_f32_16x16x32_bf16 v[110:113], v[172:175], v[216:219], v[110:113]
	v_mfma_f32_16x16x32_bf16 v[102:105], v[180:183], v[216:219], v[102:105]
	v_mfma_f32_16x16x32_bf16 v[94:97], v[172:175], v[224:227], v[94:97]
	v_mfma_f32_16x16x32_bf16 v[86:89], v[180:183], v[224:227], v[86:89]
	v_mfma_f32_16x16x32_bf16 v[78:81], v[172:175], v[232:235], v[78:81]
	v_mfma_f32_16x16x32_bf16 v[70:73], v[180:183], v[232:235], v[70:73]
	v_mfma_f32_16x16x32_bf16 v[122:125], v[184:187], v[200:203], v[122:125]
	v_mfma_f32_16x16x32_bf16 v[114:117], v[192:195], v[200:203], v[114:117]
	v_mfma_f32_16x16x32_bf16 v[106:109], v[184:187], v[208:211], v[106:109]
	v_mfma_f32_16x16x32_bf16 v[98:101], v[192:195], v[208:211], v[98:101]
	v_mfma_f32_16x16x32_bf16 v[90:93], v[184:187], v[220:223], v[90:93]
	v_mfma_f32_16x16x32_bf16 v[82:85], v[192:195], v[220:223], v[82:85]
	v_mfma_f32_16x16x32_bf16 v[74:77], v[184:187], v[228:231], v[74:77]
	v_mfma_f32_16x16x32_bf16 v[66:69], v[192:195], v[228:231], v[66:69]
	v_mfma_f32_16x16x32_bf16 v[122:125], v[188:191], v[204:207], v[122:125]
	v_mfma_f32_16x16x32_bf16 v[114:117], v[196:199], v[204:207], v[114:117]
	v_mfma_f32_16x16x32_bf16 v[106:109], v[188:191], v[216:219], v[106:109]
	v_mfma_f32_16x16x32_bf16 v[98:101], v[196:199], v[216:219], v[98:101]
	v_mfma_f32_16x16x32_bf16 v[90:93], v[188:191], v[224:227], v[90:93]
	v_mfma_f32_16x16x32_bf16 v[82:85], v[196:199], v[224:227], v[82:85]
	v_mfma_f32_16x16x32_bf16 v[74:77], v[188:191], v[232:235], v[74:77]
	v_mfma_f32_16x16x32_bf16 v[66:69], v[196:199], v[232:235], v[66:69]
	s_setprio 0
	s_barrier
	s_mov_b32 m0, s71
	v_lshl_add_u64 v[236:237], v[156:157], 0, v[134:135]
	ds_read_b128 v[200:203], v164 offset:16384
	ds_read_b128 v[204:207], v164 offset:17408
	ds_read_b128 v[208:211], v164 offset:18432
	ds_read_b128 v[216:219], v164 offset:19456
	ds_read_b128 v[220:223], v164 offset:20480
	ds_read_b128 v[224:227], v164 offset:21504
	ds_read_b128 v[228:231], v164 offset:22528
	ds_read_b128 v[232:235], v164 offset:23552
	global_load_lds_dwordx4 v[236:237], off
	v_lshl_add_u64 v[238:239], v[156:157], 0, v[132:133]
	s_mov_b32 m0, s72
	v_lshl_add_u64 v[240:241], v[156:157], 0, s[12:13]
	s_add_i32 s75, s57, s33
	global_load_lds_dwordx4 v[238:239], off
	v_lshl_add_u64 v[242:243], v[240:241], 0, v[134:135]
	s_mov_b32 m0, s75
	v_lshl_add_u64 v[240:241], v[240:241], 0, v[132:133]
	global_load_lds_dwordx4 v[242:243], off
	s_add_i32 m0, s75, 0x2000
	v_mov_b32_e32 v213, v137
	global_load_lds_dwordx4 v[240:241], off
	s_mov_b32 m0, s29
	v_lshl_add_u64 v[240:241], s[30:31], 0, v[136:137]
	global_load_lds_dwordx4 v136, s[30:31]
	s_mov_b32 m0, s40
	s_nop 0
	global_load_lds_dwordx4 v212, s[30:31]
	s_waitcnt vmcnt(8)
	s_waitcnt lgkmcnt(0)
	v_lshl_add_u64 v[212:213], s[30:31], 0, v[212:213]
	s_barrier
	s_setprio 1
	s_waitcnt lgkmcnt(0)
	v_mfma_f32_16x16x32_bf16 v[62:65], v[168:171], v[200:203], v[62:65]
	v_mfma_f32_16x16x32_bf16 v[54:57], v[176:179], v[200:203], v[54:57]
	v_mfma_f32_16x16x32_bf16 v[46:49], v[168:171], v[208:211], v[46:49]
	v_mfma_f32_16x16x32_bf16 v[38:41], v[176:179], v[208:211], v[38:41]
	v_mfma_f32_16x16x32_bf16 v[26:29], v[168:171], v[220:223], v[26:29]
	v_mfma_f32_16x16x32_bf16 v[18:21], v[176:179], v[220:223], v[18:21]
	v_mfma_f32_16x16x32_bf16 v[6:9], v[168:171], v[228:231], v[6:9]
	v_mfma_f32_16x16x32_bf16 v[2:5], v[176:179], v[228:231], v[2:5]
	v_mfma_f32_16x16x32_bf16 v[62:65], v[172:175], v[204:207], v[62:65]
	v_mfma_f32_16x16x32_bf16 v[54:57], v[180:183], v[204:207], v[54:57]
	v_mfma_f32_16x16x32_bf16 v[46:49], v[172:175], v[216:219], v[46:49]
	v_mfma_f32_16x16x32_bf16 v[38:41], v[180:183], v[216:219], v[38:41]
	v_mfma_f32_16x16x32_bf16 v[26:29], v[172:175], v[224:227], v[26:29]
	v_mfma_f32_16x16x32_bf16 v[18:21], v[180:183], v[224:227], v[18:21]
	v_mfma_f32_16x16x32_bf16 v[6:9], v[172:175], v[232:235], v[6:9]
	v_mfma_f32_16x16x32_bf16 v[2:5], v[180:183], v[232:235], v[2:5]
	v_mfma_f32_16x16x32_bf16 v[58:61], v[184:187], v[200:203], v[58:61]
	v_mfma_f32_16x16x32_bf16 v[50:53], v[192:195], v[200:203], v[50:53]
	v_mfma_f32_16x16x32_bf16 v[42:45], v[184:187], v[208:211], v[42:45]
	v_mfma_f32_16x16x32_bf16 v[30:33], v[192:195], v[208:211], v[30:33]
	v_mfma_f32_16x16x32_bf16 v[34:37], v[184:187], v[220:223], v[34:37]
	v_mfma_f32_16x16x32_bf16 v[22:25], v[192:195], v[220:223], v[22:25]
	v_mfma_f32_16x16x32_bf16 v[14:17], v[184:187], v[228:231], v[14:17]
	v_mfma_f32_16x16x32_bf16 v[10:13], v[192:195], v[228:231], v[10:13]
	v_mfma_f32_16x16x32_bf16 v[58:61], v[188:191], v[204:207], v[58:61]
	v_mfma_f32_16x16x32_bf16 v[50:53], v[196:199], v[204:207], v[50:53]
	v_mfma_f32_16x16x32_bf16 v[42:45], v[188:191], v[216:219], v[42:45]
	v_mfma_f32_16x16x32_bf16 v[30:33], v[196:199], v[216:219], v[30:33]
	v_mfma_f32_16x16x32_bf16 v[34:37], v[188:191], v[224:227], v[34:37]
	v_mfma_f32_16x16x32_bf16 v[22:25], v[196:199], v[224:227], v[22:25]
	v_mfma_f32_16x16x32_bf16 v[14:17], v[188:191], v[232:235], v[14:17]
	v_mfma_f32_16x16x32_bf16 v[10:13], v[196:199], v[232:235], v[10:13]
	s_setprio 0
	s_barrier
	s_add_i32 s75, 0, 0x18000
	v_add_u32_e32 v136, s75, v162
	s_add_i32 s76, 0, 0x1c000
	ds_read_b128 v[168:171], v136
	ds_read_b128 v[172:175], v136 offset:1024
	ds_read_b128 v[176:179], v136 offset:2048
	ds_read_b128 v[180:183], v136 offset:3072
	v_add_u32_e32 v136, s76, v162
	ds_read_b128 v[184:187], v136
	ds_read_b128 v[188:191], v136 offset:1024
	ds_read_b128 v[192:195], v136 offset:2048
	ds_read_b128 v[196:199], v136 offset:3072
	s_mov_b32 m0, s41
	ds_read_b128 v[200:203], v164 offset:32768
	ds_read_b128 v[204:207], v164 offset:33792
	ds_read_b128 v[208:211], v164 offset:34816
	ds_read_b128 v[216:219], v164 offset:35840
	ds_read_b128 v[220:223], v164 offset:36864
	ds_read_b128 v[224:227], v164 offset:37888
	ds_read_b128 v[228:231], v164 offset:38912
	ds_read_b128 v[232:235], v164 offset:39936
	global_load_lds_dwordx4 v145, s[30:31]
	s_mov_b32 m0, s42
	s_nop 0
	global_load_lds_dwordx4 v149, s[30:31]
	s_waitcnt vmcnt(8)
	s_waitcnt lgkmcnt(0)
	s_barrier
	s_setprio 1
	s_waitcnt lgkmcnt(0)
	v_mfma_f32_16x16x32_bf16 v[126:129], v[168:171], v[200:203], v[126:129]
	v_mfma_f32_16x16x32_bf16 v[118:121], v[176:179], v[200:203], v[118:121]
	v_mfma_f32_16x16x32_bf16 v[110:113], v[168:171], v[208:211], v[110:113]
	v_mfma_f32_16x16x32_bf16 v[102:105], v[176:179], v[208:211], v[102:105]
	v_mfma_f32_16x16x32_bf16 v[94:97], v[168:171], v[220:223], v[94:97]
	v_mfma_f32_16x16x32_bf16 v[86:89], v[176:179], v[220:223], v[86:89]
	v_mfma_f32_16x16x32_bf16 v[78:81], v[168:171], v[228:231], v[78:81]
	v_mfma_f32_16x16x32_bf16 v[70:73], v[176:179], v[228:231], v[70:73]
	v_mfma_f32_16x16x32_bf16 v[126:129], v[172:175], v[204:207], v[126:129]
	v_mfma_f32_16x16x32_bf16 v[118:121], v[180:183], v[204:207], v[118:121]
	v_mfma_f32_16x16x32_bf16 v[110:113], v[172:175], v[216:219], v[110:113]
	v_mfma_f32_16x16x32_bf16 v[102:105], v[180:183], v[216:219], v[102:105]
	v_mfma_f32_16x16x32_bf16 v[94:97], v[172:175], v[224:227], v[94:97]
	v_mfma_f32_16x16x32_bf16 v[86:89], v[180:183], v[224:227], v[86:89]
	v_mfma_f32_16x16x32_bf16 v[78:81], v[172:175], v[232:235], v[78:81]
	v_mfma_f32_16x16x32_bf16 v[70:73], v[180:183], v[232:235], v[70:73]
	v_mfma_f32_16x16x32_bf16 v[122:125], v[184:187], v[200:203], v[122:125]
	v_mfma_f32_16x16x32_bf16 v[114:117], v[192:195], v[200:203], v[114:117]
	v_mfma_f32_16x16x32_bf16 v[106:109], v[184:187], v[208:211], v[106:109]
	v_mfma_f32_16x16x32_bf16 v[98:101], v[192:195], v[208:211], v[98:101]
	v_mfma_f32_16x16x32_bf16 v[90:93], v[184:187], v[220:223], v[90:93]
	v_mfma_f32_16x16x32_bf16 v[82:85], v[192:195], v[220:223], v[82:85]
	v_mfma_f32_16x16x32_bf16 v[74:77], v[184:187], v[228:231], v[74:77]
	v_mfma_f32_16x16x32_bf16 v[66:69], v[192:195], v[228:231], v[66:69]
	v_mfma_f32_16x16x32_bf16 v[122:125], v[188:191], v[204:207], v[122:125]
	v_mfma_f32_16x16x32_bf16 v[114:117], v[196:199], v[204:207], v[114:117]
	v_mfma_f32_16x16x32_bf16 v[106:109], v[188:191], v[216:219], v[106:109]
	v_mfma_f32_16x16x32_bf16 v[98:101], v[196:199], v[216:219], v[98:101]
	v_mfma_f32_16x16x32_bf16 v[90:93], v[188:191], v[224:227], v[90:93]
	v_mfma_f32_16x16x32_bf16 v[82:85], v[196:199], v[224:227], v[82:85]
	v_mfma_f32_16x16x32_bf16 v[74:77], v[188:191], v[232:235], v[74:77]
	v_mfma_f32_16x16x32_bf16 v[66:69], v[196:199], v[232:235], v[66:69]
	s_setprio 0
	s_barrier
	s_add_i32 s30, s75, s33
	v_lshl_add_u64 v[236:237], v[236:237], 0, s[18:19]
	s_mov_b32 m0, s30
	ds_read_b128 v[200:203], v164 offset:49152
	ds_read_b128 v[204:207], v164 offset:50176
	ds_read_b128 v[208:211], v164 offset:51200
	ds_read_b128 v[216:219], v164 offset:52224
	ds_read_b128 v[220:223], v164 offset:53248
	ds_read_b128 v[224:227], v164 offset:54272
	ds_read_b128 v[228:231], v164 offset:55296
	ds_read_b128 v[232:235], v164 offset:56320
	global_load_lds_dwordx4 v[236:237], off
	v_lshl_add_u64 v[236:237], v[238:239], 0, s[18:19]
	s_add_i32 m0, s30, 0x2000
	v_lshl_add_u64 v[156:157], v[156:157], 0, s[22:23]
	s_add_i32 s30, s76, s33
	global_load_lds_dwordx4 v[236:237], off
	v_lshl_add_u64 v[236:237], v[156:157], 0, v[134:135]
	s_mov_b32 m0, s30
	v_lshl_add_u64 v[156:157], v[156:157], 0, v[132:133]
	global_load_lds_dwordx4 v[236:237], off
	s_add_i32 m0, s30, 0x2000
	s_nop 0
	global_load_lds_dwordx4 v[156:157], off
	v_lshl_add_u64 v[156:157], v[240:241], 0, s[18:19]
	s_mov_b32 m0, s43
	s_nop 0
	global_load_lds_dwordx4 v[156:157], off
	v_lshl_add_u64 v[156:157], v[212:213], 0, s[18:19]
	s_mov_b32 m0, s44
	s_nop 0
	global_load_lds_dwordx4 v[156:157], off
	s_waitcnt vmcnt(8)
	s_waitcnt lgkmcnt(0)
	s_barrier
	s_setprio 1
	s_waitcnt lgkmcnt(0)
	v_mfma_f32_16x16x32_bf16 v[62:65], v[168:171], v[200:203], v[62:65]
	v_mfma_f32_16x16x32_bf16 v[54:57], v[176:179], v[200:203], v[54:57]
	v_mfma_f32_16x16x32_bf16 v[46:49], v[168:171], v[208:211], v[46:49]
	v_mfma_f32_16x16x32_bf16 v[38:41], v[176:179], v[208:211], v[38:41]
	v_mfma_f32_16x16x32_bf16 v[26:29], v[168:171], v[220:223], v[26:29]
	v_mfma_f32_16x16x32_bf16 v[18:21], v[176:179], v[220:223], v[18:21]
	v_mfma_f32_16x16x32_bf16 v[6:9], v[168:171], v[228:231], v[6:9]
	v_mfma_f32_16x16x32_bf16 v[2:5], v[176:179], v[228:231], v[2:5]
	v_mfma_f32_16x16x32_bf16 v[62:65], v[172:175], v[204:207], v[62:65]
	v_mfma_f32_16x16x32_bf16 v[54:57], v[180:183], v[204:207], v[54:57]
	v_mfma_f32_16x16x32_bf16 v[46:49], v[172:175], v[216:219], v[46:49]
	v_mfma_f32_16x16x32_bf16 v[38:41], v[180:183], v[216:219], v[38:41]
	v_mfma_f32_16x16x32_bf16 v[26:29], v[172:175], v[224:227], v[26:29]
	v_mfma_f32_16x16x32_bf16 v[18:21], v[180:183], v[224:227], v[18:21]
	v_mfma_f32_16x16x32_bf16 v[6:9], v[172:175], v[232:235], v[6:9]
	v_mfma_f32_16x16x32_bf16 v[2:5], v[180:183], v[232:235], v[2:5]
	v_mfma_f32_16x16x32_bf16 v[58:61], v[184:187], v[200:203], v[58:61]
	v_mfma_f32_16x16x32_bf16 v[50:53], v[192:195], v[200:203], v[50:53]
	v_mfma_f32_16x16x32_bf16 v[42:45], v[184:187], v[208:211], v[42:45]
	v_mfma_f32_16x16x32_bf16 v[30:33], v[192:195], v[208:211], v[30:33]
	v_mfma_f32_16x16x32_bf16 v[34:37], v[184:187], v[220:223], v[34:37]
	v_mfma_f32_16x16x32_bf16 v[22:25], v[192:195], v[220:223], v[22:25]
	v_mfma_f32_16x16x32_bf16 v[14:17], v[184:187], v[228:231], v[14:17]
	v_mfma_f32_16x16x32_bf16 v[10:13], v[192:195], v[228:231], v[10:13]
	v_mfma_f32_16x16x32_bf16 v[58:61], v[188:191], v[204:207], v[58:61]
	v_mfma_f32_16x16x32_bf16 v[50:53], v[196:199], v[204:207], v[50:53]
	v_mfma_f32_16x16x32_bf16 v[42:45], v[188:191], v[216:219], v[42:45]
	v_mfma_f32_16x16x32_bf16 v[30:33], v[196:199], v[216:219], v[30:33]
	v_mfma_f32_16x16x32_bf16 v[34:37], v[188:191], v[224:227], v[34:37]
	v_mfma_f32_16x16x32_bf16 v[22:25], v[196:199], v[224:227], v[22:25]
	v_mfma_f32_16x16x32_bf16 v[14:17], v[188:191], v[232:235], v[14:17]
	v_mfma_f32_16x16x32_bf16 v[10:13], v[196:199], v[232:235], v[10:13]
	s_setprio 0
	s_barrier
	s_add_i32 s27, s27, 2
	s_add_u32 s6, s6, 0x100
	s_addc_u32 s7, s7, 0
	s_cmp_gt_u32 s27, 29
	s_cbranch_scc0 .LBB0_1065
	s_and_b64 vcc, exec, s[24:25]
	s_cbranch_vccz .LBB0_1068
	s_barrier

.LBB0_1213:
	v_add_u32_e32 v147, s57, v164
	ds_read_b128 v[176:179], v147
	ds_read_b128 v[180:183], v147 offset:1024
	ds_read_b128 v[184:187], v147 offset:2048
	ds_read_b128 v[188:191], v147 offset:3072
	v_add_u32_e32 v147, s58, v164
	s_add_u32 s36, s84, s6
	ds_read_b128 v[192:195], v147
	ds_read_b128 v[196:199], v147 offset:1024
	ds_read_b128 v[200:203], v147 offset:2048
	ds_read_b128 v[204:207], v147 offset:3072
	s_addc_u32 s37, s85, s7
	s_add_u32 s69, s36, 0x29700100
	s_addc_u32 s70, s37, 0
	s_cmpk_eq_i32 s6, 0x700
	s_cselect_b64 vcc, -1, 0
	v_lshl_add_u64 v[208:209], v[158:159], 0, s[6:7]
	s_and_b64 s[36:37], vcc, exec
	v_cndmask_b32_e32 v136, v138, v141, vcc
	s_cselect_b32 s37, s9, s70
	s_cselect_b32 s36, s8, s69
	v_cndmask_b32_e32 v142, v150, v172, vcc
	v_cndmask_b32_e32 v212, v148, v173, vcc
	v_cndmask_b32_e32 v147, v152, v174, vcc
	v_cndmask_b32_e32 v245, v209, v145, vcc
	v_cndmask_b32_e32 v244, v208, v144, vcc
	v_lshl_add_u64 v[246:247], v[156:157], 0, s[6:7]
	s_add_i32 m0, s35, 0xc000
	ds_read_b128 v[208:211], v169
	ds_read_b128 v[216:219], v169 offset:1024
	ds_read_b128 v[220:223], v169 offset:2048
	ds_read_b128 v[224:227], v169 offset:3072
	ds_read_b128 v[228:231], v169 offset:4096
	ds_read_b128 v[232:235], v169 offset:5120
	ds_read_b128 v[236:239], v169 offset:6144
	ds_read_b128 v[240:243], v169 offset:7168
	global_load_lds_dwordx4 v[246:247], off
	v_lshl_add_u64 v[246:247], v[154:155], 0, s[6:7]
	s_add_i32 m0, s35, 0xe000
	s_nop 0
	global_load_lds_dwordx4 v[246:247], off
	s_waitcnt vmcnt(8)
	s_waitcnt lgkmcnt(0)
	s_barrier
	s_setprio 1
	s_waitcnt lgkmcnt(0)
	v_mfma_f32_16x16x32_bf16 v[126:129], v[176:179], v[208:211], v[126:129]
	v_mfma_f32_16x16x32_bf16 v[122:125], v[184:187], v[208:211], v[122:125]
	v_mfma_f32_16x16x32_bf16 v[110:113], v[176:179], v[220:223], v[110:113]
	v_mfma_f32_16x16x32_bf16 v[106:109], v[184:187], v[220:223], v[106:109]
	v_mfma_f32_16x16x32_bf16 v[94:97], v[176:179], v[228:231], v[94:97]
	v_mfma_f32_16x16x32_bf16 v[90:93], v[184:187], v[228:231], v[90:93]
	v_mfma_f32_16x16x32_bf16 v[78:81], v[176:179], v[236:239], v[78:81]
	v_mfma_f32_16x16x32_bf16 v[74:77], v[184:187], v[236:239], v[74:77]
	v_mfma_f32_16x16x32_bf16 v[126:129], v[180:183], v[216:219], v[126:129]
	v_mfma_f32_16x16x32_bf16 v[122:125], v[188:191], v[216:219], v[122:125]
	v_mfma_f32_16x16x32_bf16 v[110:113], v[180:183], v[224:227], v[110:113]
	v_mfma_f32_16x16x32_bf16 v[106:109], v[188:191], v[224:227], v[106:109]
	v_mfma_f32_16x16x32_bf16 v[94:97], v[180:183], v[232:235], v[94:97]
	v_mfma_f32_16x16x32_bf16 v[90:93], v[188:191], v[232:235], v[90:93]
	v_mfma_f32_16x16x32_bf16 v[78:81], v[180:183], v[240:243], v[78:81]
	v_mfma_f32_16x16x32_bf16 v[74:77], v[188:191], v[240:243], v[74:77]
	v_mfma_f32_16x16x32_bf16 v[118:121], v[192:195], v[208:211], v[118:121]
	v_mfma_f32_16x16x32_bf16 v[114:117], v[200:203], v[208:211], v[114:117]
	v_mfma_f32_16x16x32_bf16 v[102:105], v[192:195], v[220:223], v[102:105]
	v_mfma_f32_16x16x32_bf16 v[98:101], v[200:203], v[220:223], v[98:101]
	v_mfma_f32_16x16x32_bf16 v[86:89], v[192:195], v[228:231], v[86:89]
	v_mfma_f32_16x16x32_bf16 v[82:85], v[200:203], v[228:231], v[82:85]
	v_mfma_f32_16x16x32_bf16 v[70:73], v[192:195], v[236:239], v[70:73]
	v_mfma_f32_16x16x32_bf16 v[66:69], v[200:203], v[236:239], v[66:69]
	v_mfma_f32_16x16x32_bf16 v[118:121], v[196:199], v[216:219], v[118:121]
	v_mfma_f32_16x16x32_bf16 v[114:117], v[204:207], v[216:219], v[114:117]
	v_mfma_f32_16x16x32_bf16 v[102:105], v[196:199], v[224:227], v[102:105]
	v_mfma_f32_16x16x32_bf16 v[98:101], v[204:207], v[224:227], v[98:101]
	v_mfma_f32_16x16x32_bf16 v[86:89], v[196:199], v[232:235], v[86:89]
	v_mfma_f32_16x16x32_bf16 v[82:85], v[204:207], v[232:235], v[82:85]
	v_mfma_f32_16x16x32_bf16 v[70:73], v[196:199], v[240:243], v[70:73]
	v_mfma_f32_16x16x32_bf16 v[66:69], v[204:207], v[240:243], v[66:69]
	s_setprio 0
	s_barrier
	s_add_i32 s69, s57, s39
	v_lshl_add_u64 v[246:247], v[244:245], 0, v[132:133]
	s_mov_b32 m0, s69
	ds_read_b128 v[208:211], v169 offset:16384
	ds_read_b128 v[216:219], v169 offset:17408
	ds_read_b128 v[220:223], v169 offset:18432
	ds_read_b128 v[224:227], v169 offset:19456
	ds_read_b128 v[228:231], v169 offset:20480
	ds_read_b128 v[232:235], v169 offset:21504
	ds_read_b128 v[236:239], v169 offset:22528
	ds_read_b128 v[240:243], v169 offset:23552
	global_load_lds_dwordx4 v[246:247], off
	v_lshl_add_u64 v[248:249], v[244:245], 0, v[134:135]
	s_add_i32 m0, s69, 0x2000
	v_lshl_add_u64 v[250:251], v[244:245], 0, s[10:11]
	s_add_i32 s69, s58, s39
	global_load_lds_dwordx4 v[248:249], off
	v_lshl_add_u64 v[252:253], v[250:251], 0, v[132:133]
	s_mov_b32 m0, s69
	v_lshl_add_u64 v[250:251], v[250:251], 0, v[134:135]
	global_load_lds_dwordx4 v[252:253], off
	s_add_i32 m0, s69, 0x2000
	v_mov_b32_e32 v213, v137
	global_load_lds_dwordx4 v[250:251], off
	s_mov_b32 m0, s35
	v_lshl_add_u64 v[250:251], s[36:37], 0, v[136:137]
	global_load_lds_dwordx4 v136, s[36:37]
	s_mov_b32 m0, s40
	s_nop 0
	global_load_lds_dwordx4 v212, s[36:37]
	s_waitcnt vmcnt(8)
	s_waitcnt lgkmcnt(0)
	v_lshl_add_u64 v[212:213], s[36:37], 0, v[212:213]
	s_barrier
	s_setprio 1
	s_waitcnt lgkmcnt(0)
	v_mfma_f32_16x16x32_bf16 v[62:65], v[176:179], v[208:211], v[62:65]
	v_mfma_f32_16x16x32_bf16 v[58:61], v[184:187], v[208:211], v[58:61]
	v_mfma_f32_16x16x32_bf16 v[46:49], v[176:179], v[220:223], v[46:49]
	v_mfma_f32_16x16x32_bf16 v[42:45], v[184:187], v[220:223], v[42:45]
	v_mfma_f32_16x16x32_bf16 v[14:17], v[176:179], v[228:231], v[14:17]
	v_mfma_f32_16x16x32_bf16 v[10:13], v[184:187], v[228:231], v[10:13]
	v_mfma_f32_16x16x32_bf16 v[6:9], v[176:179], v[236:239], v[6:9]
	v_mfma_f32_16x16x32_bf16 v[2:5], v[184:187], v[236:239], v[2:5]
	v_mfma_f32_16x16x32_bf16 v[62:65], v[180:183], v[216:219], v[62:65]
	v_mfma_f32_16x16x32_bf16 v[58:61], v[188:191], v[216:219], v[58:61]
	v_mfma_f32_16x16x32_bf16 v[46:49], v[180:183], v[224:227], v[46:49]
	v_mfma_f32_16x16x32_bf16 v[42:45], v[188:191], v[224:227], v[42:45]
	v_mfma_f32_16x16x32_bf16 v[14:17], v[180:183], v[232:235], v[14:17]
	v_mfma_f32_16x16x32_bf16 v[10:13], v[188:191], v[232:235], v[10:13]
	v_mfma_f32_16x16x32_bf16 v[6:9], v[180:183], v[240:243], v[6:9]
	v_mfma_f32_16x16x32_bf16 v[2:5], v[188:191], v[240:243], v[2:5]
	v_mfma_f32_16x16x32_bf16 v[54:57], v[192:195], v[208:211], v[54:57]
	v_mfma_f32_16x16x32_bf16 v[50:53], v[200:203], v[208:211], v[50:53]
	v_mfma_f32_16x16x32_bf16 v[30:33], v[192:195], v[220:223], v[30:33]
	v_mfma_f32_16x16x32_bf16 v[26:29], v[200:203], v[220:223], v[26:29]
	v_mfma_f32_16x16x32_bf16 v[34:37], v[192:195], v[228:231], v[34:37]
	v_mfma_f32_16x16x32_bf16 v[38:41], v[200:203], v[228:231], v[38:41]
	v_mfma_f32_16x16x32_bf16 v[18:21], v[192:195], v[236:239], v[18:21]
	v_mfma_f32_16x16x32_bf16 v[22:25], v[200:203], v[236:239], v[22:25]
	v_mfma_f32_16x16x32_bf16 v[54:57], v[196:199], v[216:219], v[54:57]
	v_mfma_f32_16x16x32_bf16 v[50:53], v[204:207], v[216:219], v[50:53]
	v_mfma_f32_16x16x32_bf16 v[30:33], v[196:199], v[224:227], v[30:33]
	v_mfma_f32_16x16x32_bf16 v[26:29], v[204:207], v[224:227], v[26:29]
	v_mfma_f32_16x16x32_bf16 v[34:37], v[196:199], v[232:235], v[34:37]
	v_mfma_f32_16x16x32_bf16 v[38:41], v[204:207], v[232:235], v[38:41]
	v_mfma_f32_16x16x32_bf16 v[18:21], v[196:199], v[240:243], v[18:21]
	v_mfma_f32_16x16x32_bf16 v[22:25], v[204:207], v[240:243], v[22:25]
	s_setprio 0
	s_barrier
	s_add_i32 s69, 0, 0x18000
	v_add_u32_e32 v136, s69, v164
	s_add_i32 s70, 0, 0x1c000
	ds_read_b128 v[176:179], v136
	ds_read_b128 v[180:183], v136 offset:1024
	ds_read_b128 v[184:187], v136 offset:2048
	ds_read_b128 v[188:191], v136 offset:3072
	v_add_u32_e32 v136, s70, v164
	ds_read_b128 v[192:195], v136
	ds_read_b128 v[196:199], v136 offset:1024
	ds_read_b128 v[200:203], v136 offset:2048
	ds_read_b128 v[204:207], v136 offset:3072
	s_mov_b32 m0, s41
	ds_read_b128 v[208:211], v169 offset:32768
	ds_read_b128 v[216:219], v169 offset:33792
	ds_read_b128 v[220:223], v169 offset:34816
	ds_read_b128 v[224:227], v169 offset:35840
	ds_read_b128 v[228:231], v169 offset:36864
	ds_read_b128 v[232:235], v169 offset:37888
	ds_read_b128 v[236:239], v169 offset:38912
	ds_read_b128 v[240:243], v169 offset:39936
	global_load_lds_dwordx4 v142, s[36:37]
	s_mov_b32 m0, s42
	s_nop 0
	global_load_lds_dwordx4 v147, s[36:37]
	s_waitcnt vmcnt(8)
	s_waitcnt lgkmcnt(0)
	s_barrier
	s_setprio 1
	s_waitcnt lgkmcnt(0)
	v_mfma_f32_16x16x32_bf16 v[126:129], v[176:179], v[208:211], v[126:129]
	v_mfma_f32_16x16x32_bf16 v[122:125], v[184:187], v[208:211], v[122:125]
	v_mfma_f32_16x16x32_bf16 v[110:113], v[176:179], v[220:223], v[110:113]
	v_mfma_f32_16x16x32_bf16 v[106:109], v[184:187], v[220:223], v[106:109]
	v_mfma_f32_16x16x32_bf16 v[94:97], v[176:179], v[228:231], v[94:97]
	v_mfma_f32_16x16x32_bf16 v[90:93], v[184:187], v[228:231], v[90:93]
	v_mfma_f32_16x16x32_bf16 v[78:81], v[176:179], v[236:239], v[78:81]
	v_mfma_f32_16x16x32_bf16 v[74:77], v[184:187], v[236:239], v[74:77]
	v_mfma_f32_16x16x32_bf16 v[126:129], v[180:183], v[216:219], v[126:129]
	v_mfma_f32_16x16x32_bf16 v[122:125], v[188:191], v[216:219], v[122:125]
	v_mfma_f32_16x16x32_bf16 v[110:113], v[180:183], v[224:227], v[110:113]
	v_mfma_f32_16x16x32_bf16 v[106:109], v[188:191], v[224:227], v[106:109]
	v_mfma_f32_16x16x32_bf16 v[94:97], v[180:183], v[232:235], v[94:97]
	v_mfma_f32_16x16x32_bf16 v[90:93], v[188:191], v[232:235], v[90:93]
	v_mfma_f32_16x16x32_bf16 v[78:81], v[180:183], v[240:243], v[78:81]
	v_mfma_f32_16x16x32_bf16 v[74:77], v[188:191], v[240:243], v[74:77]
	v_mfma_f32_16x16x32_bf16 v[118:121], v[192:195], v[208:211], v[118:121]
	v_mfma_f32_16x16x32_bf16 v[114:117], v[200:203], v[208:211], v[114:117]
	v_mfma_f32_16x16x32_bf16 v[102:105], v[192:195], v[220:223], v[102:105]
	v_mfma_f32_16x16x32_bf16 v[98:101], v[200:203], v[220:223], v[98:101]
	v_mfma_f32_16x16x32_bf16 v[86:89], v[192:195], v[228:231], v[86:89]
	v_mfma_f32_16x16x32_bf16 v[82:85], v[200:203], v[228:231], v[82:85]
	v_mfma_f32_16x16x32_bf16 v[70:73], v[192:195], v[236:239], v[70:73]
	v_mfma_f32_16x16x32_bf16 v[66:69], v[200:203], v[236:239], v[66:69]
	v_mfma_f32_16x16x32_bf16 v[118:121], v[196:199], v[216:219], v[118:121]
	v_mfma_f32_16x16x32_bf16 v[114:117], v[204:207], v[216:219], v[114:117]
	v_mfma_f32_16x16x32_bf16 v[102:105], v[196:199], v[224:227], v[102:105]
	v_mfma_f32_16x16x32_bf16 v[98:101], v[204:207], v[224:227], v[98:101]
	v_mfma_f32_16x16x32_bf16 v[86:89], v[196:199], v[232:235], v[86:89]
	v_mfma_f32_16x16x32_bf16 v[82:85], v[204:207], v[232:235], v[82:85]
	v_mfma_f32_16x16x32_bf16 v[70:73], v[196:199], v[240:243], v[70:73]
	v_mfma_f32_16x16x32_bf16 v[66:69], v[204:207], v[240:243], v[66:69]
	s_setprio 0
	s_barrier
	s_add_i32 s36, s69, s39
	v_lshl_add_u64 v[246:247], v[246:247], 0, s[20:21]
	s_mov_b32 m0, s36
	ds_read_b128 v[208:211], v169 offset:49152
	ds_read_b128 v[216:219], v169 offset:50176
	ds_read_b128 v[220:223], v169 offset:51200
	ds_read_b128 v[224:227], v169 offset:52224
	ds_read_b128 v[228:231], v169 offset:53248
	ds_read_b128 v[232:235], v169 offset:54272
	ds_read_b128 v[236:239], v169 offset:55296
	ds_read_b128 v[240:243], v169 offset:56320
	global_load_lds_dwordx4 v[246:247], off
	v_lshl_add_u64 v[246:247], v[248:249], 0, s[20:21]
	s_add_i32 m0, s36, 0x2000
	v_lshl_add_u64 v[244:245], v[244:245], 0, s[24:25]
	s_add_i32 s36, s70, s39
	global_load_lds_dwordx4 v[246:247], off
	v_lshl_add_u64 v[246:247], v[244:245], 0, v[132:133]
	s_mov_b32 m0, s36
	v_lshl_add_u64 v[244:245], v[244:245], 0, v[134:135]
	global_load_lds_dwordx4 v[246:247], off
	s_add_i32 m0, s36, 0x2000
	v_lshl_add_u64 v[212:213], v[212:213], 0, s[20:21]
	global_load_lds_dwordx4 v[244:245], off
	v_lshl_add_u64 v[244:245], v[250:251], 0, s[20:21]
	s_mov_b32 m0, s44
	s_nop 0
	global_load_lds_dwordx4 v[244:245], off
	s_mov_b32 m0, s45
	s_nop 0
	global_load_lds_dwordx4 v[212:213], off
	s_waitcnt vmcnt(8)
	s_waitcnt lgkmcnt(0)
	s_barrier
	s_setprio 1
	s_waitcnt lgkmcnt(0)
	v_mfma_f32_16x16x32_bf16 v[62:65], v[176:179], v[208:211], v[62:65]
	v_mfma_f32_16x16x32_bf16 v[58:61], v[184:187], v[208:211], v[58:61]
	v_mfma_f32_16x16x32_bf16 v[46:49], v[176:179], v[220:223], v[46:49]
	v_mfma_f32_16x16x32_bf16 v[42:45], v[184:187], v[220:223], v[42:45]
	v_mfma_f32_16x16x32_bf16 v[14:17], v[176:179], v[228:231], v[14:17]
	v_mfma_f32_16x16x32_bf16 v[10:13], v[184:187], v[228:231], v[10:13]
	v_mfma_f32_16x16x32_bf16 v[6:9], v[176:179], v[236:239], v[6:9]
	v_mfma_f32_16x16x32_bf16 v[2:5], v[184:187], v[236:239], v[2:5]
	v_mfma_f32_16x16x32_bf16 v[62:65], v[180:183], v[216:219], v[62:65]
	v_mfma_f32_16x16x32_bf16 v[58:61], v[188:191], v[216:219], v[58:61]
	v_mfma_f32_16x16x32_bf16 v[46:49], v[180:183], v[224:227], v[46:49]
	v_mfma_f32_16x16x32_bf16 v[42:45], v[188:191], v[224:227], v[42:45]
	v_mfma_f32_16x16x32_bf16 v[14:17], v[180:183], v[232:235], v[14:17]
	v_mfma_f32_16x16x32_bf16 v[10:13], v[188:191], v[232:235], v[10:13]
	v_mfma_f32_16x16x32_bf16 v[6:9], v[180:183], v[240:243], v[6:9]
	v_mfma_f32_16x16x32_bf16 v[2:5], v[188:191], v[240:243], v[2:5]
	v_mfma_f32_16x16x32_bf16 v[54:57], v[192:195], v[208:211], v[54:57]
	v_mfma_f32_16x16x32_bf16 v[50:53], v[200:203], v[208:211], v[50:53]
	v_mfma_f32_16x16x32_bf16 v[30:33], v[192:195], v[220:223], v[30:33]
	v_mfma_f32_16x16x32_bf16 v[26:29], v[200:203], v[220:223], v[26:29]
	v_mfma_f32_16x16x32_bf16 v[34:37], v[192:195], v[228:231], v[34:37]
	v_mfma_f32_16x16x32_bf16 v[38:41], v[200:203], v[228:231], v[38:41]
	v_mfma_f32_16x16x32_bf16 v[18:21], v[192:195], v[236:239], v[18:21]
	v_mfma_f32_16x16x32_bf16 v[22:25], v[200:203], v[236:239], v[22:25]
	v_mfma_f32_16x16x32_bf16 v[54:57], v[196:199], v[216:219], v[54:57]
	v_mfma_f32_16x16x32_bf16 v[50:53], v[204:207], v[216:219], v[50:53]
	v_mfma_f32_16x16x32_bf16 v[30:33], v[196:199], v[224:227], v[30:33]
	v_mfma_f32_16x16x32_bf16 v[26:29], v[204:207], v[224:227], v[26:29]
	v_mfma_f32_16x16x32_bf16 v[34:37], v[196:199], v[232:235], v[34:37]
	v_mfma_f32_16x16x32_bf16 v[38:41], v[204:207], v[232:235], v[38:41]
	v_mfma_f32_16x16x32_bf16 v[18:21], v[196:199], v[240:243], v[18:21]
	v_mfma_f32_16x16x32_bf16 v[22:25], v[204:207], v[240:243], v[22:25]
	s_setprio 0
	s_barrier
	s_add_i32 s31, s31, 2
	s_add_u32 s6, s6, 0x100
	s_addc_u32 s7, s7, 0
	s_cmp_gt_u32 s31, 13
	s_cbranch_scc0 .LBB0_1213
	s_and_b64 vcc, exec, s[26:27]
	s_cbranch_vccz .LBB0_1216
	s_barrier

.LBB0_1447:
	ds_read_b128 v[170:173], v162
	ds_read_b128 v[174:177], v162 offset:1024
	ds_read_b128 v[178:181], v162 offset:2048
	ds_read_b128 v[182:185], v162 offset:3072
	ds_read_b128 v[186:189], v163
	ds_read_b128 v[190:193], v163 offset:1024
	ds_read_b128 v[194:197], v163 offset:2048
	ds_read_b128 v[198:201], v163 offset:3072
	s_add_u32 s22, s84, s20
	s_addc_u32 s23, s85, s21
	s_add_u32 s24, s22, 0x100
	s_addc_u32 s25, s23, 0
	s_add_u32 s48, s19, s20
	s_addc_u32 s49, s26, s21
	s_cmpk_eq_i32 s20, 0xf00
	s_cselect_b64 vcc, -1, 0
	s_and_b64 s[22:23], vcc, exec
	v_cndmask_b32_e32 v134, v146, v166, vcc
	s_cselect_b32 s25, s85, s25
	s_cselect_b32 s24, s84, s24
	v_cndmask_b32_e32 v147, v150, v167, vcc
	v_cndmask_b32_e32 v238, v148, v168, vcc
	v_cndmask_b32_e32 v151, v152, v169, vcc
	s_cselect_b32 s23, s7, s49
	s_cselect_b32 s22, s6, s48
	v_lshl_add_u64 v[240:241], v[156:157], 0, s[20:21]
	s_add_i32 m0, s31, 0xc000
	ds_read_b128 v[202:205], v164
	ds_read_b128 v[206:209], v164 offset:1024
	ds_read_b128 v[210:213], v164 offset:2048
	ds_read_b128 v[218:221], v164 offset:3072
	ds_read_b128 v[222:225], v164 offset:4096
	ds_read_b128 v[226:229], v164 offset:5120
	ds_read_b128 v[230:233], v164 offset:6144
	ds_read_b128 v[234:237], v164 offset:7168
	global_load_lds_dwordx4 v[240:241], off
	v_lshl_add_u64 v[240:241], v[154:155], 0, s[20:21]
	s_add_i32 m0, s31, 0xe000
	s_nop 0
	global_load_lds_dwordx4 v[240:241], off
	s_waitcnt vmcnt(8)
	s_waitcnt lgkmcnt(0)
	s_barrier
	s_setprio 1
	s_waitcnt lgkmcnt(0)
	v_mfma_f32_16x16x32_bf16 v[126:129], v[170:173], v[202:205], v[126:129]
	v_mfma_f32_16x16x32_bf16 v[122:125], v[178:181], v[202:205], v[122:125]
	v_mfma_f32_16x16x32_bf16 v[118:121], v[170:173], v[210:213], v[118:121]
	v_mfma_f32_16x16x32_bf16 v[110:113], v[178:181], v[210:213], v[110:113]
	v_mfma_f32_16x16x32_bf16 v[102:105], v[170:173], v[222:225], v[102:105]
	v_mfma_f32_16x16x32_bf16 v[94:97], v[178:181], v[222:225], v[94:97]
	v_mfma_f32_16x16x32_bf16 v[86:89], v[170:173], v[230:233], v[86:89]
	v_mfma_f32_16x16x32_bf16 v[78:81], v[178:181], v[230:233], v[78:81]
	v_mfma_f32_16x16x32_bf16 v[126:129], v[174:177], v[206:209], v[126:129]
	v_mfma_f32_16x16x32_bf16 v[122:125], v[182:185], v[206:209], v[122:125]
	v_mfma_f32_16x16x32_bf16 v[118:121], v[174:177], v[218:221], v[118:121]
	v_mfma_f32_16x16x32_bf16 v[110:113], v[182:185], v[218:221], v[110:113]
	v_mfma_f32_16x16x32_bf16 v[102:105], v[174:177], v[226:229], v[102:105]
	v_mfma_f32_16x16x32_bf16 v[94:97], v[182:185], v[226:229], v[94:97]
	v_mfma_f32_16x16x32_bf16 v[86:89], v[174:177], v[234:237], v[86:89]
	v_mfma_f32_16x16x32_bf16 v[78:81], v[182:185], v[234:237], v[78:81]
	v_mfma_f32_16x16x32_bf16 v[114:117], v[186:189], v[202:205], v[114:117]
	v_mfma_f32_16x16x32_bf16 v[106:109], v[194:197], v[202:205], v[106:109]
	v_mfma_f32_16x16x32_bf16 v[98:101], v[186:189], v[210:213], v[98:101]
	v_mfma_f32_16x16x32_bf16 v[90:93], v[194:197], v[210:213], v[90:93]
	v_mfma_f32_16x16x32_bf16 v[82:85], v[186:189], v[222:225], v[82:85]
	v_mfma_f32_16x16x32_bf16 v[74:77], v[194:197], v[222:225], v[74:77]
	v_mfma_f32_16x16x32_bf16 v[70:73], v[186:189], v[230:233], v[70:73]
	v_mfma_f32_16x16x32_bf16 v[66:69], v[194:197], v[230:233], v[66:69]
	v_mfma_f32_16x16x32_bf16 v[114:117], v[190:193], v[206:209], v[114:117]
	v_mfma_f32_16x16x32_bf16 v[106:109], v[198:201], v[206:209], v[106:109]
	v_mfma_f32_16x16x32_bf16 v[98:101], v[190:193], v[218:221], v[98:101]
	v_mfma_f32_16x16x32_bf16 v[90:93], v[198:201], v[218:221], v[90:93]
	v_mfma_f32_16x16x32_bf16 v[82:85], v[190:193], v[226:229], v[82:85]
	v_mfma_f32_16x16x32_bf16 v[74:77], v[198:201], v[226:229], v[74:77]
	v_mfma_f32_16x16x32_bf16 v[70:73], v[190:193], v[234:237], v[70:73]
	v_mfma_f32_16x16x32_bf16 v[66:69], v[198:201], v[234:237], v[66:69]
	s_setprio 0
	s_barrier
	s_add_i32 s48, s40, s2
	v_lshl_add_u64 v[240:241], s[22:23], 0, v[132:133]
	s_mov_b32 m0, s48
	ds_read_b128 v[202:205], v164 offset:16384
	ds_read_b128 v[206:209], v164 offset:17408
	ds_read_b128 v[210:213], v164 offset:18432
	ds_read_b128 v[218:221], v164 offset:19456
	ds_read_b128 v[222:225], v164 offset:20480
	ds_read_b128 v[226:229], v164 offset:21504
	ds_read_b128 v[230:233], v164 offset:22528
	ds_read_b128 v[234:237], v164 offset:23552
	global_load_lds_dwordx4 v[240:241], off
	s_add_i32 m0, s48, 0x2000
	s_add_u32 s48, s22, 0x80000
	v_lshl_add_u64 v[242:243], s[22:23], 0, v[130:131]
	s_addc_u32 s49, s23, 0
	s_add_i32 s50, s41, s2
	global_load_lds_dwordx4 v[242:243], off
	v_lshl_add_u64 v[244:245], s[48:49], 0, v[132:133]
	s_mov_b32 m0, s50
	v_mov_b32_e32 v239, v135
	global_load_lds_dwordx4 v[244:245], off
	v_lshl_add_u64 v[244:245], s[48:49], 0, v[130:131]
	s_add_i32 m0, s50, 0x2000
	s_nop 0
	global_load_lds_dwordx4 v[244:245], off
	s_mov_b32 m0, s31
	v_lshl_add_u64 v[244:245], s[24:25], 0, v[134:135]
	global_load_lds_dwordx4 v134, s[24:25]
	s_mov_b32 m0, s33
	s_nop 0
	global_load_lds_dwordx4 v238, s[24:25]
	s_waitcnt vmcnt(8)
	s_waitcnt lgkmcnt(0)
	v_lshl_add_u64 v[238:239], s[24:25], 0, v[238:239]
	s_barrier
	s_setprio 1
	s_waitcnt lgkmcnt(0)
	v_mfma_f32_16x16x32_bf16 v[62:65], v[170:173], v[202:205], v[62:65]
	v_mfma_f32_16x16x32_bf16 v[58:61], v[178:181], v[202:205], v[58:61]
	v_mfma_f32_16x16x32_bf16 v[46:49], v[170:173], v[210:213], v[46:49]
	v_mfma_f32_16x16x32_bf16 v[30:33], v[178:181], v[210:213], v[30:33]
	v_mfma_f32_16x16x32_bf16 v[22:25], v[170:173], v[222:225], v[22:25]
	v_mfma_f32_16x16x32_bf16 v[14:17], v[178:181], v[222:225], v[14:17]
	v_mfma_f32_16x16x32_bf16 v[6:9], v[170:173], v[230:233], v[6:9]
	v_mfma_f32_16x16x32_bf16 v[2:5], v[178:181], v[230:233], v[2:5]
	v_mfma_f32_16x16x32_bf16 v[62:65], v[174:177], v[206:209], v[62:65]
	v_mfma_f32_16x16x32_bf16 v[58:61], v[182:185], v[206:209], v[58:61]
	v_mfma_f32_16x16x32_bf16 v[46:49], v[174:177], v[218:221], v[46:49]
	v_mfma_f32_16x16x32_bf16 v[30:33], v[182:185], v[218:221], v[30:33]
	v_mfma_f32_16x16x32_bf16 v[22:25], v[174:177], v[226:229], v[22:25]
	v_mfma_f32_16x16x32_bf16 v[14:17], v[182:185], v[226:229], v[14:17]
	v_mfma_f32_16x16x32_bf16 v[6:9], v[174:177], v[234:237], v[6:9]
	v_mfma_f32_16x16x32_bf16 v[2:5], v[182:185], v[234:237], v[2:5]
	v_mfma_f32_16x16x32_bf16 v[38:41], v[186:189], v[202:205], v[38:41]
	v_mfma_f32_16x16x32_bf16 v[26:29], v[194:197], v[202:205], v[26:29]
	v_mfma_f32_16x16x32_bf16 v[18:21], v[186:189], v[210:213], v[18:21]
	v_mfma_f32_16x16x32_bf16 v[10:13], v[194:197], v[210:213], v[10:13]
	v_mfma_f32_16x16x32_bf16 v[54:57], v[186:189], v[222:225], v[54:57]
	v_mfma_f32_16x16x32_bf16 v[50:53], v[194:197], v[222:225], v[50:53]
	v_mfma_f32_16x16x32_bf16 v[42:45], v[186:189], v[230:233], v[42:45]
	v_mfma_f32_16x16x32_bf16 v[34:37], v[194:197], v[230:233], v[34:37]
	v_mfma_f32_16x16x32_bf16 v[38:41], v[190:193], v[206:209], v[38:41]
	v_mfma_f32_16x16x32_bf16 v[26:29], v[198:201], v[206:209], v[26:29]
	v_mfma_f32_16x16x32_bf16 v[18:21], v[190:193], v[218:221], v[18:21]
	v_mfma_f32_16x16x32_bf16 v[10:13], v[198:201], v[218:221], v[10:13]
	v_mfma_f32_16x16x32_bf16 v[54:57], v[190:193], v[226:229], v[54:57]
	v_mfma_f32_16x16x32_bf16 v[50:53], v[198:201], v[226:229], v[50:53]
	v_mfma_f32_16x16x32_bf16 v[42:45], v[190:193], v[234:237], v[42:45]
	v_mfma_f32_16x16x32_bf16 v[34:37], v[198:201], v[234:237], v[34:37]
	s_setprio 0
	s_barrier
	s_add_i32 s48, 0, 0x18000
	v_add_u32_e32 v134, s48, v161
	s_add_i32 s49, 0, 0x1c000
	ds_read_b128 v[170:173], v134
	ds_read_b128 v[174:177], v134 offset:1024
	ds_read_b128 v[178:181], v134 offset:2048
	ds_read_b128 v[182:185], v134 offset:3072
	v_add_u32_e32 v134, s49, v161
	ds_read_b128 v[186:189], v134
	ds_read_b128 v[190:193], v134 offset:1024
	ds_read_b128 v[194:197], v134 offset:2048
	ds_read_b128 v[198:201], v134 offset:3072
	s_mov_b32 m0, s34
	ds_read_b128 v[202:205], v164 offset:32768
	ds_read_b128 v[206:209], v164 offset:33792
	ds_read_b128 v[210:213], v164 offset:34816
	ds_read_b128 v[218:221], v164 offset:35840
	ds_read_b128 v[222:225], v164 offset:36864
	ds_read_b128 v[226:229], v164 offset:37888
	ds_read_b128 v[230:233], v164 offset:38912
	ds_read_b128 v[234:237], v164 offset:39936
	global_load_lds_dwordx4 v147, s[24:25]
	s_mov_b32 m0, s35
	s_nop 0
	global_load_lds_dwordx4 v151, s[24:25]
	s_waitcnt vmcnt(8)
	s_waitcnt lgkmcnt(0)
	s_barrier
	s_setprio 1
	s_waitcnt lgkmcnt(0)
	v_mfma_f32_16x16x32_bf16 v[126:129], v[170:173], v[202:205], v[126:129]
	v_mfma_f32_16x16x32_bf16 v[122:125], v[178:181], v[202:205], v[122:125]
	v_mfma_f32_16x16x32_bf16 v[118:121], v[170:173], v[210:213], v[118:121]
	v_mfma_f32_16x16x32_bf16 v[110:113], v[178:181], v[210:213], v[110:113]
	v_mfma_f32_16x16x32_bf16 v[102:105], v[170:173], v[222:225], v[102:105]
	v_mfma_f32_16x16x32_bf16 v[94:97], v[178:181], v[222:225], v[94:97]
	v_mfma_f32_16x16x32_bf16 v[86:89], v[170:173], v[230:233], v[86:89]
	v_mfma_f32_16x16x32_bf16 v[78:81], v[178:181], v[230:233], v[78:81]
	v_mfma_f32_16x16x32_bf16 v[126:129], v[174:177], v[206:209], v[126:129]
	v_mfma_f32_16x16x32_bf16 v[122:125], v[182:185], v[206:209], v[122:125]
	v_mfma_f32_16x16x32_bf16 v[118:121], v[174:177], v[218:221], v[118:121]
	v_mfma_f32_16x16x32_bf16 v[110:113], v[182:185], v[218:221], v[110:113]
	v_mfma_f32_16x16x32_bf16 v[102:105], v[174:177], v[226:229], v[102:105]
	v_mfma_f32_16x16x32_bf16 v[94:97], v[182:185], v[226:229], v[94:97]
	v_mfma_f32_16x16x32_bf16 v[86:89], v[174:177], v[234:237], v[86:89]
	v_mfma_f32_16x16x32_bf16 v[78:81], v[182:185], v[234:237], v[78:81]
	v_mfma_f32_16x16x32_bf16 v[114:117], v[186:189], v[202:205], v[114:117]
	v_mfma_f32_16x16x32_bf16 v[106:109], v[194:197], v[202:205], v[106:109]
	v_mfma_f32_16x16x32_bf16 v[98:101], v[186:189], v[210:213], v[98:101]
	v_mfma_f32_16x16x32_bf16 v[90:93], v[194:197], v[210:213], v[90:93]
	v_mfma_f32_16x16x32_bf16 v[82:85], v[186:189], v[222:225], v[82:85]
	v_mfma_f32_16x16x32_bf16 v[74:77], v[194:197], v[222:225], v[74:77]
	v_mfma_f32_16x16x32_bf16 v[70:73], v[186:189], v[230:233], v[70:73]
	v_mfma_f32_16x16x32_bf16 v[66:69], v[194:197], v[230:233], v[66:69]
	v_mfma_f32_16x16x32_bf16 v[114:117], v[190:193], v[206:209], v[114:117]
	v_mfma_f32_16x16x32_bf16 v[106:109], v[198:201], v[206:209], v[106:109]
	v_mfma_f32_16x16x32_bf16 v[98:101], v[190:193], v[218:221], v[98:101]
	v_mfma_f32_16x16x32_bf16 v[90:93], v[198:201], v[218:221], v[90:93]
	v_mfma_f32_16x16x32_bf16 v[82:85], v[190:193], v[226:229], v[82:85]
	v_mfma_f32_16x16x32_bf16 v[74:77], v[198:201], v[226:229], v[74:77]
	v_mfma_f32_16x16x32_bf16 v[70:73], v[190:193], v[234:237], v[70:73]
	v_mfma_f32_16x16x32_bf16 v[66:69], v[198:201], v[234:237], v[66:69]
	s_setprio 0
	s_barrier
	s_add_i32 s24, s48, s2
	v_lshl_add_u64 v[240:241], v[240:241], 0, s[12:13]
	s_mov_b32 m0, s24
	ds_read_b128 v[202:205], v164 offset:49152
	ds_read_b128 v[206:209], v164 offset:50176
	ds_read_b128 v[210:213], v164 offset:51200
	ds_read_b128 v[218:221], v164 offset:52224
	ds_read_b128 v[222:225], v164 offset:53248
	ds_read_b128 v[226:229], v164 offset:54272
	ds_read_b128 v[230:233], v164 offset:55296
	ds_read_b128 v[234:237], v164 offset:56320
	global_load_lds_dwordx4 v[240:241], off
	s_add_i32 m0, s24, 0x2000
	s_add_u32 s22, s22, 0x80080
	v_lshl_add_u64 v[240:241], v[242:243], 0, s[12:13]
	s_addc_u32 s23, s23, 0
	s_add_i32 s24, s49, s2
	global_load_lds_dwordx4 v[240:241], off
	v_lshl_add_u64 v[240:241], s[22:23], 0, v[132:133]
	s_mov_b32 m0, s24
	v_lshl_add_u64 v[238:239], v[238:239], 0, s[12:13]
	global_load_lds_dwordx4 v[240:241], off
	v_lshl_add_u64 v[240:241], s[22:23], 0, v[130:131]
	s_add_i32 m0, s24, 0x2000
	s_nop 0
	global_load_lds_dwordx4 v[240:241], off
	v_lshl_add_u64 v[240:241], v[244:245], 0, s[12:13]
	s_mov_b32 m0, s37
	s_nop 0
	global_load_lds_dwordx4 v[240:241], off
	s_mov_b32 m0, s38
	s_nop 0
	global_load_lds_dwordx4 v[238:239], off
	s_waitcnt vmcnt(8)
	s_waitcnt lgkmcnt(0)
	s_barrier
	s_setprio 1
	s_waitcnt lgkmcnt(0)
	v_mfma_f32_16x16x32_bf16 v[62:65], v[170:173], v[202:205], v[62:65]
	v_mfma_f32_16x16x32_bf16 v[58:61], v[178:181], v[202:205], v[58:61]
	v_mfma_f32_16x16x32_bf16 v[46:49], v[170:173], v[210:213], v[46:49]
	v_mfma_f32_16x16x32_bf16 v[30:33], v[178:181], v[210:213], v[30:33]
	v_mfma_f32_16x16x32_bf16 v[22:25], v[170:173], v[222:225], v[22:25]
	v_mfma_f32_16x16x32_bf16 v[14:17], v[178:181], v[222:225], v[14:17]
	v_mfma_f32_16x16x32_bf16 v[6:9], v[170:173], v[230:233], v[6:9]
	v_mfma_f32_16x16x32_bf16 v[2:5], v[178:181], v[230:233], v[2:5]
	v_mfma_f32_16x16x32_bf16 v[62:65], v[174:177], v[206:209], v[62:65]
	v_mfma_f32_16x16x32_bf16 v[58:61], v[182:185], v[206:209], v[58:61]
	v_mfma_f32_16x16x32_bf16 v[46:49], v[174:177], v[218:221], v[46:49]
	v_mfma_f32_16x16x32_bf16 v[30:33], v[182:185], v[218:221], v[30:33]
	v_mfma_f32_16x16x32_bf16 v[22:25], v[174:177], v[226:229], v[22:25]
	v_mfma_f32_16x16x32_bf16 v[14:17], v[182:185], v[226:229], v[14:17]
	v_mfma_f32_16x16x32_bf16 v[6:9], v[174:177], v[234:237], v[6:9]
	v_mfma_f32_16x16x32_bf16 v[2:5], v[182:185], v[234:237], v[2:5]
	v_mfma_f32_16x16x32_bf16 v[38:41], v[186:189], v[202:205], v[38:41]
	v_mfma_f32_16x16x32_bf16 v[26:29], v[194:197], v[202:205], v[26:29]
	v_mfma_f32_16x16x32_bf16 v[18:21], v[186:189], v[210:213], v[18:21]
	v_mfma_f32_16x16x32_bf16 v[10:13], v[194:197], v[210:213], v[10:13]
	v_mfma_f32_16x16x32_bf16 v[54:57], v[186:189], v[222:225], v[54:57]
	v_mfma_f32_16x16x32_bf16 v[50:53], v[194:197], v[222:225], v[50:53]
	v_mfma_f32_16x16x32_bf16 v[42:45], v[186:189], v[230:233], v[42:45]
	v_mfma_f32_16x16x32_bf16 v[34:37], v[194:197], v[230:233], v[34:37]
	v_mfma_f32_16x16x32_bf16 v[38:41], v[190:193], v[206:209], v[38:41]
	v_mfma_f32_16x16x32_bf16 v[26:29], v[198:201], v[206:209], v[26:29]
	v_mfma_f32_16x16x32_bf16 v[18:21], v[190:193], v[218:221], v[18:21]
	v_mfma_f32_16x16x32_bf16 v[10:13], v[198:201], v[218:221], v[10:13]
	v_mfma_f32_16x16x32_bf16 v[54:57], v[190:193], v[226:229], v[54:57]
	v_mfma_f32_16x16x32_bf16 v[50:53], v[198:201], v[226:229], v[50:53]
	v_mfma_f32_16x16x32_bf16 v[42:45], v[190:193], v[234:237], v[42:45]
	v_mfma_f32_16x16x32_bf16 v[34:37], v[198:201], v[234:237], v[34:37]
	s_setprio 0
	s_barrier
	s_add_i32 s27, s27, 2
	s_add_u32 s20, s20, 0x100
	s_addc_u32 s21, s21, 0
	s_cmp_gt_u32 s27, 29
	s_cbranch_scc0 .LBB0_1447
	s_and_b64 vcc, exec, s[14:15]
	s_cbranch_vccz .LBB0_1450
	s_barrier

.LBB0_1758:
	ds_read_b128 v[164:167], v156
	ds_read_b128 v[168:171], v156 offset:1024
	ds_read_b128 v[172:175], v156 offset:2048
	ds_read_b128 v[176:179], v156 offset:3072
	ds_read_b128 v[180:183], v157
	ds_read_b128 v[184:187], v157 offset:1024
	ds_read_b128 v[188:191], v157 offset:2048
	ds_read_b128 v[192:195], v157 offset:3072
	s_add_u32 s34, s84, s30
	s_addc_u32 s35, s85, s31
	s_add_u32 s36, s34, 0x25300100
	s_addc_u32 s37, s35, 0
	s_add_u32 s60, s29, s30
	s_addc_u32 s61, s58, s31
	s_cmpk_eq_i32 s30, 0xf00
	s_cselect_b64 vcc, -1, 0
	s_and_b64 s[34:35], vcc, exec
	v_cndmask_b32_e32 v134, v141, v159, vcc
	s_cselect_b32 s37, s9, s37
	s_cselect_b32 s36, s8, s36
	v_cndmask_b32_e32 v143, v142, v160, vcc
	v_cndmask_b32_e32 v212, v140, v161, vcc
	v_cndmask_b32_e32 v145, v144, v162, vcc
	s_cselect_b32 s35, s7, s61
	s_cselect_b32 s34, s6, s60
	v_lshl_add_u64 v[234:235], v[148:149], 0, s[30:31]
	s_add_i32 m0, s40, 0xc000
	ds_read_b128 v[196:199], v158
	ds_read_b128 v[200:203], v158 offset:1024
	ds_read_b128 v[204:207], v158 offset:2048
	ds_read_b128 v[208:211], v158 offset:3072
	ds_read_b128 v[218:221], v158 offset:4096
	ds_read_b128 v[222:225], v158 offset:5120
	ds_read_b128 v[226:229], v158 offset:6144
	ds_read_b128 v[230:233], v158 offset:7168
	global_load_lds_dwordx4 v[234:235], off
	v_lshl_add_u64 v[234:235], v[146:147], 0, s[30:31]
	s_add_i32 m0, s40, 0xe000
	s_nop 0
	global_load_lds_dwordx4 v[234:235], off
	s_waitcnt vmcnt(8)
	s_waitcnt lgkmcnt(0)
	s_barrier
	s_setprio 1
	s_waitcnt lgkmcnt(0)
	v_mfma_f32_16x16x32_bf16 v[126:129], v[164:167], v[196:199], v[126:129]
	v_mfma_f32_16x16x32_bf16 v[122:125], v[172:175], v[196:199], v[122:125]
	v_mfma_f32_16x16x32_bf16 v[118:121], v[164:167], v[204:207], v[118:121]
	v_mfma_f32_16x16x32_bf16 v[110:113], v[172:175], v[204:207], v[110:113]
	v_mfma_f32_16x16x32_bf16 v[102:105], v[164:167], v[218:221], v[102:105]
	v_mfma_f32_16x16x32_bf16 v[94:97], v[172:175], v[218:221], v[94:97]
	v_mfma_f32_16x16x32_bf16 v[86:89], v[164:167], v[226:229], v[86:89]
	v_mfma_f32_16x16x32_bf16 v[78:81], v[172:175], v[226:229], v[78:81]
	v_mfma_f32_16x16x32_bf16 v[126:129], v[168:171], v[200:203], v[126:129]
	v_mfma_f32_16x16x32_bf16 v[122:125], v[176:179], v[200:203], v[122:125]
	v_mfma_f32_16x16x32_bf16 v[118:121], v[168:171], v[208:211], v[118:121]
	v_mfma_f32_16x16x32_bf16 v[110:113], v[176:179], v[208:211], v[110:113]
	v_mfma_f32_16x16x32_bf16 v[102:105], v[168:171], v[222:225], v[102:105]
	v_mfma_f32_16x16x32_bf16 v[94:97], v[176:179], v[222:225], v[94:97]
	v_mfma_f32_16x16x32_bf16 v[86:89], v[168:171], v[230:233], v[86:89]
	v_mfma_f32_16x16x32_bf16 v[78:81], v[176:179], v[230:233], v[78:81]
	v_mfma_f32_16x16x32_bf16 v[114:117], v[180:183], v[196:199], v[114:117]
	v_mfma_f32_16x16x32_bf16 v[106:109], v[188:191], v[196:199], v[106:109]
	v_mfma_f32_16x16x32_bf16 v[98:101], v[180:183], v[204:207], v[98:101]
	v_mfma_f32_16x16x32_bf16 v[90:93], v[188:191], v[204:207], v[90:93]
	v_mfma_f32_16x16x32_bf16 v[82:85], v[180:183], v[218:221], v[82:85]
	v_mfma_f32_16x16x32_bf16 v[74:77], v[188:191], v[218:221], v[74:77]
	v_mfma_f32_16x16x32_bf16 v[70:73], v[180:183], v[226:229], v[70:73]
	v_mfma_f32_16x16x32_bf16 v[66:69], v[188:191], v[226:229], v[66:69]
	v_mfma_f32_16x16x32_bf16 v[114:117], v[184:187], v[200:203], v[114:117]
	v_mfma_f32_16x16x32_bf16 v[106:109], v[192:195], v[200:203], v[106:109]
	v_mfma_f32_16x16x32_bf16 v[98:101], v[184:187], v[208:211], v[98:101]
	v_mfma_f32_16x16x32_bf16 v[90:93], v[192:195], v[208:211], v[90:93]
	v_mfma_f32_16x16x32_bf16 v[82:85], v[184:187], v[222:225], v[82:85]
	v_mfma_f32_16x16x32_bf16 v[74:77], v[192:195], v[222:225], v[74:77]
	v_mfma_f32_16x16x32_bf16 v[70:73], v[184:187], v[230:233], v[70:73]
	v_mfma_f32_16x16x32_bf16 v[66:69], v[192:195], v[230:233], v[66:69]
	s_setprio 0
	s_barrier
	s_add_i32 s60, s49, s39
	v_lshl_add_u64 v[234:235], s[34:35], 0, v[130:131]
	s_mov_b32 m0, s60
	ds_read_b128 v[196:199], v158 offset:16384
	ds_read_b128 v[200:203], v158 offset:17408
	ds_read_b128 v[204:207], v158 offset:18432
	ds_read_b128 v[208:211], v158 offset:19456
	ds_read_b128 v[218:221], v158 offset:20480
	ds_read_b128 v[222:225], v158 offset:21504
	ds_read_b128 v[226:229], v158 offset:22528
	ds_read_b128 v[230:233], v158 offset:23552
	global_load_lds_dwordx4 v[234:235], off
	s_add_i32 m0, s60, 0x2000
	s_add_u32 s60, s34, 0x80000
	v_lshl_add_u64 v[236:237], s[34:35], 0, v[132:133]
	s_addc_u32 s61, s35, 0
	s_add_i32 s62, s50, s39
	global_load_lds_dwordx4 v[236:237], off
	v_lshl_add_u64 v[238:239], s[60:61], 0, v[130:131]
	s_mov_b32 m0, s62
	v_mov_b32_e32 v213, v135
	global_load_lds_dwordx4 v[238:239], off
	v_lshl_add_u64 v[238:239], s[60:61], 0, v[132:133]
	s_add_i32 m0, s62, 0x2000
	s_nop 0
	global_load_lds_dwordx4 v[238:239], off
	s_mov_b32 m0, s40
	v_lshl_add_u64 v[238:239], s[36:37], 0, v[134:135]
	global_load_lds_dwordx4 v134, s[36:37]
	s_mov_b32 m0, s41
	s_nop 0
	global_load_lds_dwordx4 v212, s[36:37]
	s_waitcnt vmcnt(8)
	s_waitcnt lgkmcnt(0)
	v_lshl_add_u64 v[212:213], s[36:37], 0, v[212:213]
	s_barrier
	s_setprio 1
	s_waitcnt lgkmcnt(0)
	v_mfma_f32_16x16x32_bf16 v[62:65], v[164:167], v[196:199], v[62:65]
	v_mfma_f32_16x16x32_bf16 v[58:61], v[172:175], v[196:199], v[58:61]
	v_mfma_f32_16x16x32_bf16 v[46:49], v[164:167], v[204:207], v[46:49]
	v_mfma_f32_16x16x32_bf16 v[38:41], v[172:175], v[204:207], v[38:41]
	v_mfma_f32_16x16x32_bf16 v[22:25], v[164:167], v[218:221], v[22:25]
	v_mfma_f32_16x16x32_bf16 v[14:17], v[172:175], v[218:221], v[14:17]
	v_mfma_f32_16x16x32_bf16 v[6:9], v[164:167], v[226:229], v[6:9]
	v_mfma_f32_16x16x32_bf16 v[2:5], v[172:175], v[226:229], v[2:5]
	v_mfma_f32_16x16x32_bf16 v[62:65], v[168:171], v[200:203], v[62:65]
	v_mfma_f32_16x16x32_bf16 v[58:61], v[176:179], v[200:203], v[58:61]
	v_mfma_f32_16x16x32_bf16 v[46:49], v[168:171], v[208:211], v[46:49]
	v_mfma_f32_16x16x32_bf16 v[38:41], v[176:179], v[208:211], v[38:41]
	v_mfma_f32_16x16x32_bf16 v[22:25], v[168:171], v[222:225], v[22:25]
	v_mfma_f32_16x16x32_bf16 v[14:17], v[176:179], v[222:225], v[14:17]
	v_mfma_f32_16x16x32_bf16 v[6:9], v[168:171], v[230:233], v[6:9]
	v_mfma_f32_16x16x32_bf16 v[2:5], v[176:179], v[230:233], v[2:5]
	v_mfma_f32_16x16x32_bf16 v[42:45], v[180:183], v[196:199], v[42:45]
	v_mfma_f32_16x16x32_bf16 v[30:33], v[188:191], v[196:199], v[30:33]
	v_mfma_f32_16x16x32_bf16 v[18:21], v[180:183], v[204:207], v[18:21]
	v_mfma_f32_16x16x32_bf16 v[10:13], v[188:191], v[204:207], v[10:13]
	v_mfma_f32_16x16x32_bf16 v[54:57], v[180:183], v[218:221], v[54:57]
	v_mfma_f32_16x16x32_bf16 v[50:53], v[188:191], v[218:221], v[50:53]
	v_mfma_f32_16x16x32_bf16 v[34:37], v[180:183], v[226:229], v[34:37]
	v_mfma_f32_16x16x32_bf16 v[26:29], v[188:191], v[226:229], v[26:29]
	v_mfma_f32_16x16x32_bf16 v[42:45], v[184:187], v[200:203], v[42:45]
	v_mfma_f32_16x16x32_bf16 v[30:33], v[192:195], v[200:203], v[30:33]
	v_mfma_f32_16x16x32_bf16 v[18:21], v[184:187], v[208:211], v[18:21]
	v_mfma_f32_16x16x32_bf16 v[10:13], v[192:195], v[208:211], v[10:13]
	v_mfma_f32_16x16x32_bf16 v[54:57], v[184:187], v[222:225], v[54:57]
	v_mfma_f32_16x16x32_bf16 v[50:53], v[192:195], v[222:225], v[50:53]
	v_mfma_f32_16x16x32_bf16 v[34:37], v[184:187], v[230:233], v[34:37]
	v_mfma_f32_16x16x32_bf16 v[26:29], v[192:195], v[230:233], v[26:29]
	s_setprio 0
	s_barrier
	s_add_i32 s60, 0, 0x18000
	v_add_u32_e32 v134, s60, v154
	s_add_i32 s61, 0, 0x1c000
	ds_read_b128 v[164:167], v134
	ds_read_b128 v[168:171], v134 offset:1024
	ds_read_b128 v[172:175], v134 offset:2048
	ds_read_b128 v[176:179], v134 offset:3072
	v_add_u32_e32 v134, s61, v154
	ds_read_b128 v[180:183], v134
	ds_read_b128 v[184:187], v134 offset:1024
	ds_read_b128 v[188:191], v134 offset:2048
	ds_read_b128 v[192:195], v134 offset:3072
	s_mov_b32 m0, s42
	ds_read_b128 v[196:199], v158 offset:32768
	ds_read_b128 v[200:203], v158 offset:33792
	ds_read_b128 v[204:207], v158 offset:34816
	ds_read_b128 v[208:211], v158 offset:35840
	ds_read_b128 v[218:221], v158 offset:36864
	ds_read_b128 v[222:225], v158 offset:37888
	ds_read_b128 v[226:229], v158 offset:38912
	ds_read_b128 v[230:233], v158 offset:39936
	global_load_lds_dwordx4 v143, s[36:37]
	s_mov_b32 m0, s43
	s_nop 0
	global_load_lds_dwordx4 v145, s[36:37]
	s_waitcnt vmcnt(8)
	s_waitcnt lgkmcnt(0)
	s_barrier
	s_setprio 1
	s_waitcnt lgkmcnt(0)
	v_mfma_f32_16x16x32_bf16 v[126:129], v[164:167], v[196:199], v[126:129]
	v_mfma_f32_16x16x32_bf16 v[122:125], v[172:175], v[196:199], v[122:125]
	v_mfma_f32_16x16x32_bf16 v[118:121], v[164:167], v[204:207], v[118:121]
	v_mfma_f32_16x16x32_bf16 v[110:113], v[172:175], v[204:207], v[110:113]
	v_mfma_f32_16x16x32_bf16 v[102:105], v[164:167], v[218:221], v[102:105]
	v_mfma_f32_16x16x32_bf16 v[94:97], v[172:175], v[218:221], v[94:97]
	v_mfma_f32_16x16x32_bf16 v[86:89], v[164:167], v[226:229], v[86:89]
	v_mfma_f32_16x16x32_bf16 v[78:81], v[172:175], v[226:229], v[78:81]
	v_mfma_f32_16x16x32_bf16 v[126:129], v[168:171], v[200:203], v[126:129]
	v_mfma_f32_16x16x32_bf16 v[122:125], v[176:179], v[200:203], v[122:125]
	v_mfma_f32_16x16x32_bf16 v[118:121], v[168:171], v[208:211], v[118:121]
	v_mfma_f32_16x16x32_bf16 v[110:113], v[176:179], v[208:211], v[110:113]
	v_mfma_f32_16x16x32_bf16 v[102:105], v[168:171], v[222:225], v[102:105]
	v_mfma_f32_16x16x32_bf16 v[94:97], v[176:179], v[222:225], v[94:97]
	v_mfma_f32_16x16x32_bf16 v[86:89], v[168:171], v[230:233], v[86:89]
	v_mfma_f32_16x16x32_bf16 v[78:81], v[176:179], v[230:233], v[78:81]
	v_mfma_f32_16x16x32_bf16 v[114:117], v[180:183], v[196:199], v[114:117]
	v_mfma_f32_16x16x32_bf16 v[106:109], v[188:191], v[196:199], v[106:109]
	v_mfma_f32_16x16x32_bf16 v[98:101], v[180:183], v[204:207], v[98:101]
	v_mfma_f32_16x16x32_bf16 v[90:93], v[188:191], v[204:207], v[90:93]
	v_mfma_f32_16x16x32_bf16 v[82:85], v[180:183], v[218:221], v[82:85]
	v_mfma_f32_16x16x32_bf16 v[74:77], v[188:191], v[218:221], v[74:77]
	v_mfma_f32_16x16x32_bf16 v[70:73], v[180:183], v[226:229], v[70:73]
	v_mfma_f32_16x16x32_bf16 v[66:69], v[188:191], v[226:229], v[66:69]
	v_mfma_f32_16x16x32_bf16 v[114:117], v[184:187], v[200:203], v[114:117]
	v_mfma_f32_16x16x32_bf16 v[106:109], v[192:195], v[200:203], v[106:109]
	v_mfma_f32_16x16x32_bf16 v[98:101], v[184:187], v[208:211], v[98:101]
	v_mfma_f32_16x16x32_bf16 v[90:93], v[192:195], v[208:211], v[90:93]
	v_mfma_f32_16x16x32_bf16 v[82:85], v[184:187], v[222:225], v[82:85]
	v_mfma_f32_16x16x32_bf16 v[74:77], v[192:195], v[222:225], v[74:77]
	v_mfma_f32_16x16x32_bf16 v[70:73], v[184:187], v[230:233], v[70:73]
	v_mfma_f32_16x16x32_bf16 v[66:69], v[192:195], v[230:233], v[66:69]
	s_setprio 0
	s_barrier
	s_add_i32 s36, s60, s39
	v_lshl_add_u64 v[234:235], v[234:235], 0, s[16:17]
	s_mov_b32 m0, s36
	ds_read_b128 v[196:199], v158 offset:49152
	ds_read_b128 v[200:203], v158 offset:50176
	ds_read_b128 v[204:207], v158 offset:51200
	ds_read_b128 v[208:211], v158 offset:52224
	ds_read_b128 v[218:221], v158 offset:53248
	ds_read_b128 v[222:225], v158 offset:54272
	ds_read_b128 v[226:229], v158 offset:55296
	ds_read_b128 v[230:233], v158 offset:56320
	global_load_lds_dwordx4 v[234:235], off
	s_add_i32 m0, s36, 0x2000
	s_add_u32 s34, s34, 0x80080
	v_lshl_add_u64 v[234:235], v[236:237], 0, s[16:17]
	s_addc_u32 s35, s35, 0
	s_add_i32 s36, s61, s39
	global_load_lds_dwordx4 v[234:235], off
	v_lshl_add_u64 v[234:235], s[34:35], 0, v[130:131]
	s_mov_b32 m0, s36
	v_lshl_add_u64 v[212:213], v[212:213], 0, s[16:17]
	global_load_lds_dwordx4 v[234:235], off
	v_lshl_add_u64 v[234:235], s[34:35], 0, v[132:133]
	s_add_i32 m0, s36, 0x2000
	s_nop 0
	global_load_lds_dwordx4 v[234:235], off
	v_lshl_add_u64 v[234:235], v[238:239], 0, s[16:17]
	s_mov_b32 m0, s45
	s_nop 0
	global_load_lds_dwordx4 v[234:235], off
	s_mov_b32 m0, s47
	s_nop 0
	global_load_lds_dwordx4 v[212:213], off
	s_waitcnt vmcnt(8)
	s_waitcnt lgkmcnt(0)
	s_barrier
	s_setprio 1
	s_waitcnt lgkmcnt(0)
	v_mfma_f32_16x16x32_bf16 v[62:65], v[164:167], v[196:199], v[62:65]
	v_mfma_f32_16x16x32_bf16 v[58:61], v[172:175], v[196:199], v[58:61]
	v_mfma_f32_16x16x32_bf16 v[46:49], v[164:167], v[204:207], v[46:49]
	v_mfma_f32_16x16x32_bf16 v[38:41], v[172:175], v[204:207], v[38:41]
	v_mfma_f32_16x16x32_bf16 v[22:25], v[164:167], v[218:221], v[22:25]
	v_mfma_f32_16x16x32_bf16 v[14:17], v[172:175], v[218:221], v[14:17]
	v_mfma_f32_16x16x32_bf16 v[6:9], v[164:167], v[226:229], v[6:9]
	v_mfma_f32_16x16x32_bf16 v[2:5], v[172:175], v[226:229], v[2:5]
	v_mfma_f32_16x16x32_bf16 v[62:65], v[168:171], v[200:203], v[62:65]
	v_mfma_f32_16x16x32_bf16 v[58:61], v[176:179], v[200:203], v[58:61]
	v_mfma_f32_16x16x32_bf16 v[46:49], v[168:171], v[208:211], v[46:49]
	v_mfma_f32_16x16x32_bf16 v[38:41], v[176:179], v[208:211], v[38:41]
	v_mfma_f32_16x16x32_bf16 v[22:25], v[168:171], v[222:225], v[22:25]
	v_mfma_f32_16x16x32_bf16 v[14:17], v[176:179], v[222:225], v[14:17]
	v_mfma_f32_16x16x32_bf16 v[6:9], v[168:171], v[230:233], v[6:9]
	v_mfma_f32_16x16x32_bf16 v[2:5], v[176:179], v[230:233], v[2:5]
	v_mfma_f32_16x16x32_bf16 v[42:45], v[180:183], v[196:199], v[42:45]
	v_mfma_f32_16x16x32_bf16 v[30:33], v[188:191], v[196:199], v[30:33]
	v_mfma_f32_16x16x32_bf16 v[18:21], v[180:183], v[204:207], v[18:21]
	v_mfma_f32_16x16x32_bf16 v[10:13], v[188:191], v[204:207], v[10:13]
	v_mfma_f32_16x16x32_bf16 v[54:57], v[180:183], v[218:221], v[54:57]
	v_mfma_f32_16x16x32_bf16 v[50:53], v[188:191], v[218:221], v[50:53]
	v_mfma_f32_16x16x32_bf16 v[34:37], v[180:183], v[226:229], v[34:37]
	v_mfma_f32_16x16x32_bf16 v[26:29], v[188:191], v[226:229], v[26:29]
	v_mfma_f32_16x16x32_bf16 v[42:45], v[184:187], v[200:203], v[42:45]
	v_mfma_f32_16x16x32_bf16 v[30:33], v[192:195], v[200:203], v[30:33]
	v_mfma_f32_16x16x32_bf16 v[18:21], v[184:187], v[208:211], v[18:21]
	v_mfma_f32_16x16x32_bf16 v[10:13], v[192:195], v[208:211], v[10:13]
	v_mfma_f32_16x16x32_bf16 v[54:57], v[184:187], v[222:225], v[54:57]
	v_mfma_f32_16x16x32_bf16 v[50:53], v[192:195], v[222:225], v[50:53]
	v_mfma_f32_16x16x32_bf16 v[34:37], v[184:187], v[230:233], v[34:37]
	v_mfma_f32_16x16x32_bf16 v[26:29], v[192:195], v[230:233], v[26:29]
	s_setprio 0
	s_barrier
	s_add_i32 s59, s59, 2
	s_add_u32 s30, s30, 0x100
	s_addc_u32 s31, s31, 0
	s_cmp_gt_u32 s59, 29
	s_cbranch_scc0 .LBB0_1758
	s_and_b64 vcc, exec, s[20:21]
	s_cbranch_vccz .LBB0_1761
	s_barrier

.LBB0_1913:
	v_add_u32_e32 v149, s57, v160
	ds_read_b128 v[166:169], v149
	ds_read_b128 v[170:173], v149 offset:1024
	ds_read_b128 v[174:177], v149 offset:2048
	ds_read_b128 v[178:181], v149 offset:3072
	v_add_u32_e32 v149, s58, v160
	s_add_u32 s34, s84, s6
	ds_read_b128 v[182:185], v149
	ds_read_b128 v[186:189], v149 offset:1024
	ds_read_b128 v[190:193], v149 offset:2048
	ds_read_b128 v[194:197], v149 offset:3072
	s_addc_u32 s35, s85, s7
	s_add_u32 s70, s34, 0x25300100
	s_addc_u32 s71, s35, 0
	s_cmpk_eq_i32 s6, 0xf00
	s_cselect_b64 vcc, -1, 0
	v_lshl_add_u64 v[198:199], v[154:155], 0, s[6:7]
	s_and_b64 s[34:35], vcc, exec
	v_cndmask_b32_e32 v136, v147, v139, vcc
	s_cselect_b32 s35, s11, s71
	s_cselect_b32 s34, s10, s70
	v_cndmask_b32_e32 v145, v144, v163, vcc
	v_cndmask_b32_e32 v234, v146, v164, vcc
	v_cndmask_b32_e32 v149, v148, v165, vcc
	v_cndmask_b32_e32 v237, v199, v143, vcc
	v_cndmask_b32_e32 v236, v198, v142, vcc
	s_mov_b32 m0, s62
	v_lshl_add_u64 v[238:239], v[152:153], 0, s[6:7]
	ds_read_b128 v[198:201], v162
	ds_read_b128 v[202:205], v162 offset:1024
	ds_read_b128 v[206:209], v162 offset:2048
	ds_read_b128 v[210:213], v162 offset:3072
	ds_read_b128 v[218:221], v162 offset:4096
	ds_read_b128 v[222:225], v162 offset:5120
	ds_read_b128 v[226:229], v162 offset:6144
	ds_read_b128 v[230:233], v162 offset:7168
	global_load_lds_dwordx4 v[238:239], off
	v_lshl_add_u64 v[238:239], v[150:151], 0, s[6:7]
	s_mov_b32 m0, s63
	s_nop 0
	global_load_lds_dwordx4 v[238:239], off
	s_waitcnt vmcnt(8)
	s_waitcnt lgkmcnt(0)
	s_barrier
	s_setprio 1
	s_waitcnt lgkmcnt(0)
	v_mfma_f32_16x16x32_bf16 v[126:129], v[166:169], v[198:201], v[126:129]
	v_mfma_f32_16x16x32_bf16 v[118:121], v[174:177], v[198:201], v[118:121]
	v_mfma_f32_16x16x32_bf16 v[110:113], v[166:169], v[206:209], v[110:113]
	v_mfma_f32_16x16x32_bf16 v[102:105], v[174:177], v[206:209], v[102:105]
	v_mfma_f32_16x16x32_bf16 v[94:97], v[166:169], v[218:221], v[94:97]
	v_mfma_f32_16x16x32_bf16 v[86:89], v[174:177], v[218:221], v[86:89]
	v_mfma_f32_16x16x32_bf16 v[78:81], v[166:169], v[226:229], v[78:81]
	v_mfma_f32_16x16x32_bf16 v[70:73], v[174:177], v[226:229], v[70:73]
	v_mfma_f32_16x16x32_bf16 v[126:129], v[170:173], v[202:205], v[126:129]
	v_mfma_f32_16x16x32_bf16 v[118:121], v[178:181], v[202:205], v[118:121]
	v_mfma_f32_16x16x32_bf16 v[110:113], v[170:173], v[210:213], v[110:113]
	v_mfma_f32_16x16x32_bf16 v[102:105], v[178:181], v[210:213], v[102:105]
	v_mfma_f32_16x16x32_bf16 v[94:97], v[170:173], v[222:225], v[94:97]
	v_mfma_f32_16x16x32_bf16 v[86:89], v[178:181], v[222:225], v[86:89]
	v_mfma_f32_16x16x32_bf16 v[78:81], v[170:173], v[230:233], v[78:81]
	v_mfma_f32_16x16x32_bf16 v[70:73], v[178:181], v[230:233], v[70:73]
	v_mfma_f32_16x16x32_bf16 v[122:125], v[182:185], v[198:201], v[122:125]
	v_mfma_f32_16x16x32_bf16 v[114:117], v[190:193], v[198:201], v[114:117]
	v_mfma_f32_16x16x32_bf16 v[106:109], v[182:185], v[206:209], v[106:109]
	v_mfma_f32_16x16x32_bf16 v[98:101], v[190:193], v[206:209], v[98:101]
	v_mfma_f32_16x16x32_bf16 v[90:93], v[182:185], v[218:221], v[90:93]
	v_mfma_f32_16x16x32_bf16 v[82:85], v[190:193], v[218:221], v[82:85]
	v_mfma_f32_16x16x32_bf16 v[74:77], v[182:185], v[226:229], v[74:77]
	v_mfma_f32_16x16x32_bf16 v[66:69], v[190:193], v[226:229], v[66:69]
	v_mfma_f32_16x16x32_bf16 v[122:125], v[186:189], v[202:205], v[122:125]
	v_mfma_f32_16x16x32_bf16 v[114:117], v[194:197], v[202:205], v[114:117]
	v_mfma_f32_16x16x32_bf16 v[106:109], v[186:189], v[210:213], v[106:109]
	v_mfma_f32_16x16x32_bf16 v[98:101], v[194:197], v[210:213], v[98:101]
	v_mfma_f32_16x16x32_bf16 v[90:93], v[186:189], v[222:225], v[90:93]
	v_mfma_f32_16x16x32_bf16 v[82:85], v[194:197], v[222:225], v[82:85]
	v_mfma_f32_16x16x32_bf16 v[74:77], v[186:189], v[230:233], v[74:77]
	v_mfma_f32_16x16x32_bf16 v[66:69], v[194:197], v[230:233], v[66:69]
	s_setprio 0
	s_barrier
	s_mov_b32 m0, s64
	v_lshl_add_u64 v[238:239], v[236:237], 0, v[134:135]
	ds_read_b128 v[198:201], v162 offset:16384
	ds_read_b128 v[202:205], v162 offset:17408
	ds_read_b128 v[206:209], v162 offset:18432
	ds_read_b128 v[210:213], v162 offset:19456
	ds_read_b128 v[218:221], v162 offset:20480
	ds_read_b128 v[222:225], v162 offset:21504
	ds_read_b128 v[226:229], v162 offset:22528
	ds_read_b128 v[230:233], v162 offset:23552
	global_load_lds_dwordx4 v[238:239], off
	v_lshl_add_u64 v[240:241], v[236:237], 0, v[132:133]
	s_mov_b32 m0, s65
	v_lshl_add_u64 v[242:243], v[236:237], 0, s[12:13]
	s_add_i32 s70, s58, s36
	global_load_lds_dwordx4 v[240:241], off
	v_lshl_add_u64 v[244:245], v[242:243], 0, v[134:135]
	s_mov_b32 m0, s70
	v_lshl_add_u64 v[242:243], v[242:243], 0, v[132:133]
	global_load_lds_dwordx4 v[244:245], off
	s_add_i32 m0, s70, 0x2000
	v_mov_b32_e32 v235, v137
	global_load_lds_dwordx4 v[242:243], off
	s_mov_b32 m0, s31
	v_lshl_add_u64 v[242:243], s[34:35], 0, v[136:137]
	global_load_lds_dwordx4 v136, s[34:35]
	s_mov_b32 m0, s41
	s_nop 0
	global_load_lds_dwordx4 v234, s[34:35]
	s_waitcnt vmcnt(8)
	s_waitcnt lgkmcnt(0)
	v_lshl_add_u64 v[234:235], s[34:35], 0, v[234:235]
	s_barrier
	s_setprio 1
	s_waitcnt lgkmcnt(0)
	v_mfma_f32_16x16x32_bf16 v[62:65], v[166:169], v[198:201], v[62:65]
	v_mfma_f32_16x16x32_bf16 v[54:57], v[174:177], v[198:201], v[54:57]
	v_mfma_f32_16x16x32_bf16 v[46:49], v[166:169], v[206:209], v[46:49]
	v_mfma_f32_16x16x32_bf16 v[38:41], v[174:177], v[206:209], v[38:41]
	v_mfma_f32_16x16x32_bf16 v[26:29], v[166:169], v[218:221], v[26:29]
	v_mfma_f32_16x16x32_bf16 v[18:21], v[174:177], v[218:221], v[18:21]
	v_mfma_f32_16x16x32_bf16 v[6:9], v[166:169], v[226:229], v[6:9]
	v_mfma_f32_16x16x32_bf16 v[2:5], v[174:177], v[226:229], v[2:5]
	v_mfma_f32_16x16x32_bf16 v[62:65], v[170:173], v[202:205], v[62:65]
	v_mfma_f32_16x16x32_bf16 v[54:57], v[178:181], v[202:205], v[54:57]
	v_mfma_f32_16x16x32_bf16 v[46:49], v[170:173], v[210:213], v[46:49]
	v_mfma_f32_16x16x32_bf16 v[38:41], v[178:181], v[210:213], v[38:41]
	v_mfma_f32_16x16x32_bf16 v[26:29], v[170:173], v[222:225], v[26:29]
	v_mfma_f32_16x16x32_bf16 v[18:21], v[178:181], v[222:225], v[18:21]
	v_mfma_f32_16x16x32_bf16 v[6:9], v[170:173], v[230:233], v[6:9]
	v_mfma_f32_16x16x32_bf16 v[2:5], v[178:181], v[230:233], v[2:5]
	v_mfma_f32_16x16x32_bf16 v[58:61], v[182:185], v[198:201], v[58:61]
	v_mfma_f32_16x16x32_bf16 v[50:53], v[190:193], v[198:201], v[50:53]
	v_mfma_f32_16x16x32_bf16 v[42:45], v[182:185], v[206:209], v[42:45]
	v_mfma_f32_16x16x32_bf16 v[30:33], v[190:193], v[206:209], v[30:33]
	v_mfma_f32_16x16x32_bf16 v[34:37], v[182:185], v[218:221], v[34:37]
	v_mfma_f32_16x16x32_bf16 v[22:25], v[190:193], v[218:221], v[22:25]
	v_mfma_f32_16x16x32_bf16 v[14:17], v[182:185], v[226:229], v[14:17]
	v_mfma_f32_16x16x32_bf16 v[10:13], v[190:193], v[226:229], v[10:13]
	v_mfma_f32_16x16x32_bf16 v[58:61], v[186:189], v[202:205], v[58:61]
	v_mfma_f32_16x16x32_bf16 v[50:53], v[194:197], v[202:205], v[50:53]
	v_mfma_f32_16x16x32_bf16 v[42:45], v[186:189], v[210:213], v[42:45]
	v_mfma_f32_16x16x32_bf16 v[30:33], v[194:197], v[210:213], v[30:33]
	v_mfma_f32_16x16x32_bf16 v[34:37], v[186:189], v[222:225], v[34:37]
	v_mfma_f32_16x16x32_bf16 v[22:25], v[194:197], v[222:225], v[22:25]
	v_mfma_f32_16x16x32_bf16 v[14:17], v[186:189], v[230:233], v[14:17]
	v_mfma_f32_16x16x32_bf16 v[10:13], v[194:197], v[230:233], v[10:13]
	s_setprio 0
	s_barrier
	s_add_i32 s70, 0, 0x18000
	v_add_u32_e32 v136, s70, v160
	s_add_i32 s71, 0, 0x1c000
	ds_read_b128 v[166:169], v136
	ds_read_b128 v[170:173], v136 offset:1024
	ds_read_b128 v[174:177], v136 offset:2048
	ds_read_b128 v[178:181], v136 offset:3072
	v_add_u32_e32 v136, s71, v160
	ds_read_b128 v[182:185], v136
	ds_read_b128 v[186:189], v136 offset:1024
	ds_read_b128 v[190:193], v136 offset:2048
	ds_read_b128 v[194:197], v136 offset:3072
	s_mov_b32 m0, s42
	ds_read_b128 v[198:201], v162 offset:32768
	ds_read_b128 v[202:205], v162 offset:33792
	ds_read_b128 v[206:209], v162 offset:34816
	ds_read_b128 v[210:213], v162 offset:35840
	ds_read_b128 v[218:221], v162 offset:36864
	ds_read_b128 v[222:225], v162 offset:37888
	ds_read_b128 v[226:229], v162 offset:38912
	ds_read_b128 v[230:233], v162 offset:39936
	global_load_lds_dwordx4 v145, s[34:35]
	s_mov_b32 m0, s43
	s_nop 0
	global_load_lds_dwordx4 v149, s[34:35]
	s_waitcnt vmcnt(8)
	s_waitcnt lgkmcnt(0)
	s_barrier
	s_setprio 1
	s_waitcnt lgkmcnt(0)
	v_mfma_f32_16x16x32_bf16 v[126:129], v[166:169], v[198:201], v[126:129]
	v_mfma_f32_16x16x32_bf16 v[118:121], v[174:177], v[198:201], v[118:121]
	v_mfma_f32_16x16x32_bf16 v[110:113], v[166:169], v[206:209], v[110:113]
	v_mfma_f32_16x16x32_bf16 v[102:105], v[174:177], v[206:209], v[102:105]
	v_mfma_f32_16x16x32_bf16 v[94:97], v[166:169], v[218:221], v[94:97]
	v_mfma_f32_16x16x32_bf16 v[86:89], v[174:177], v[218:221], v[86:89]
	v_mfma_f32_16x16x32_bf16 v[78:81], v[166:169], v[226:229], v[78:81]
	v_mfma_f32_16x16x32_bf16 v[70:73], v[174:177], v[226:229], v[70:73]
	v_mfma_f32_16x16x32_bf16 v[126:129], v[170:173], v[202:205], v[126:129]
	v_mfma_f32_16x16x32_bf16 v[118:121], v[178:181], v[202:205], v[118:121]
	v_mfma_f32_16x16x32_bf16 v[110:113], v[170:173], v[210:213], v[110:113]
	v_mfma_f32_16x16x32_bf16 v[102:105], v[178:181], v[210:213], v[102:105]
	v_mfma_f32_16x16x32_bf16 v[94:97], v[170:173], v[222:225], v[94:97]
	v_mfma_f32_16x16x32_bf16 v[86:89], v[178:181], v[222:225], v[86:89]
	v_mfma_f32_16x16x32_bf16 v[78:81], v[170:173], v[230:233], v[78:81]
	v_mfma_f32_16x16x32_bf16 v[70:73], v[178:181], v[230:233], v[70:73]
	v_mfma_f32_16x16x32_bf16 v[122:125], v[182:185], v[198:201], v[122:125]
	v_mfma_f32_16x16x32_bf16 v[114:117], v[190:193], v[198:201], v[114:117]
	v_mfma_f32_16x16x32_bf16 v[106:109], v[182:185], v[206:209], v[106:109]
	v_mfma_f32_16x16x32_bf16 v[98:101], v[190:193], v[206:209], v[98:101]
	v_mfma_f32_16x16x32_bf16 v[90:93], v[182:185], v[218:221], v[90:93]
	v_mfma_f32_16x16x32_bf16 v[82:85], v[190:193], v[218:221], v[82:85]
	v_mfma_f32_16x16x32_bf16 v[74:77], v[182:185], v[226:229], v[74:77]
	v_mfma_f32_16x16x32_bf16 v[66:69], v[190:193], v[226:229], v[66:69]
	v_mfma_f32_16x16x32_bf16 v[122:125], v[186:189], v[202:205], v[122:125]
	v_mfma_f32_16x16x32_bf16 v[114:117], v[194:197], v[202:205], v[114:117]
	v_mfma_f32_16x16x32_bf16 v[106:109], v[186:189], v[210:213], v[106:109]
	v_mfma_f32_16x16x32_bf16 v[98:101], v[194:197], v[210:213], v[98:101]
	v_mfma_f32_16x16x32_bf16 v[90:93], v[186:189], v[222:225], v[90:93]
	v_mfma_f32_16x16x32_bf16 v[82:85], v[194:197], v[222:225], v[82:85]
	v_mfma_f32_16x16x32_bf16 v[74:77], v[186:189], v[230:233], v[74:77]
	v_mfma_f32_16x16x32_bf16 v[66:69], v[194:197], v[230:233], v[66:69]
	s_setprio 0
	s_barrier
	s_add_i32 s34, s70, s36
	v_lshl_add_u64 v[238:239], v[238:239], 0, s[18:19]
	s_mov_b32 m0, s34
	ds_read_b128 v[198:201], v162 offset:49152
	ds_read_b128 v[202:205], v162 offset:50176
	ds_read_b128 v[206:209], v162 offset:51200
	ds_read_b128 v[210:213], v162 offset:52224
	ds_read_b128 v[218:221], v162 offset:53248
	ds_read_b128 v[222:225], v162 offset:54272
	ds_read_b128 v[226:229], v162 offset:55296
	ds_read_b128 v[230:233], v162 offset:56320
	global_load_lds_dwordx4 v[238:239], off
	v_lshl_add_u64 v[238:239], v[240:241], 0, s[18:19]
	s_add_i32 m0, s34, 0x2000
	v_lshl_add_u64 v[236:237], v[236:237], 0, s[22:23]
	s_add_i32 s34, s71, s36
	global_load_lds_dwordx4 v[238:239], off
	v_lshl_add_u64 v[238:239], v[236:237], 0, v[134:135]
	s_mov_b32 m0, s34
	v_lshl_add_u64 v[236:237], v[236:237], 0, v[132:133]
	global_load_lds_dwordx4 v[238:239], off
	s_add_i32 m0, s34, 0x2000
	v_lshl_add_u64 v[234:235], v[234:235], 0, s[18:19]
	global_load_lds_dwordx4 v[236:237], off
	v_lshl_add_u64 v[236:237], v[242:243], 0, s[18:19]
	s_mov_b32 m0, s44
	s_nop 0
	global_load_lds_dwordx4 v[236:237], off
	s_mov_b32 m0, s45
	s_nop 0
	global_load_lds_dwordx4 v[234:235], off
	s_waitcnt vmcnt(8)
	s_waitcnt lgkmcnt(0)
	s_barrier
	s_setprio 1
	s_waitcnt lgkmcnt(0)
	v_mfma_f32_16x16x32_bf16 v[62:65], v[166:169], v[198:201], v[62:65]
	v_mfma_f32_16x16x32_bf16 v[54:57], v[174:177], v[198:201], v[54:57]
	v_mfma_f32_16x16x32_bf16 v[46:49], v[166:169], v[206:209], v[46:49]
	v_mfma_f32_16x16x32_bf16 v[38:41], v[174:177], v[206:209], v[38:41]
	v_mfma_f32_16x16x32_bf16 v[26:29], v[166:169], v[218:221], v[26:29]
	v_mfma_f32_16x16x32_bf16 v[18:21], v[174:177], v[218:221], v[18:21]
	v_mfma_f32_16x16x32_bf16 v[6:9], v[166:169], v[226:229], v[6:9]
	v_mfma_f32_16x16x32_bf16 v[2:5], v[174:177], v[226:229], v[2:5]
	v_mfma_f32_16x16x32_bf16 v[62:65], v[170:173], v[202:205], v[62:65]
	v_mfma_f32_16x16x32_bf16 v[54:57], v[178:181], v[202:205], v[54:57]
	v_mfma_f32_16x16x32_bf16 v[46:49], v[170:173], v[210:213], v[46:49]
	v_mfma_f32_16x16x32_bf16 v[38:41], v[178:181], v[210:213], v[38:41]
	v_mfma_f32_16x16x32_bf16 v[26:29], v[170:173], v[222:225], v[26:29]
	v_mfma_f32_16x16x32_bf16 v[18:21], v[178:181], v[222:225], v[18:21]
	v_mfma_f32_16x16x32_bf16 v[6:9], v[170:173], v[230:233], v[6:9]
	v_mfma_f32_16x16x32_bf16 v[2:5], v[178:181], v[230:233], v[2:5]
	v_mfma_f32_16x16x32_bf16 v[58:61], v[182:185], v[198:201], v[58:61]
	v_mfma_f32_16x16x32_bf16 v[50:53], v[190:193], v[198:201], v[50:53]
	v_mfma_f32_16x16x32_bf16 v[42:45], v[182:185], v[206:209], v[42:45]
	v_mfma_f32_16x16x32_bf16 v[30:33], v[190:193], v[206:209], v[30:33]
	v_mfma_f32_16x16x32_bf16 v[34:37], v[182:185], v[218:221], v[34:37]
	v_mfma_f32_16x16x32_bf16 v[22:25], v[190:193], v[218:221], v[22:25]
	v_mfma_f32_16x16x32_bf16 v[14:17], v[182:185], v[226:229], v[14:17]
	v_mfma_f32_16x16x32_bf16 v[10:13], v[190:193], v[226:229], v[10:13]
	v_mfma_f32_16x16x32_bf16 v[58:61], v[186:189], v[202:205], v[58:61]
	v_mfma_f32_16x16x32_bf16 v[50:53], v[194:197], v[202:205], v[50:53]
	v_mfma_f32_16x16x32_bf16 v[42:45], v[186:189], v[210:213], v[42:45]
	v_mfma_f32_16x16x32_bf16 v[30:33], v[194:197], v[210:213], v[30:33]
	v_mfma_f32_16x16x32_bf16 v[34:37], v[186:189], v[222:225], v[34:37]
	v_mfma_f32_16x16x32_bf16 v[22:25], v[194:197], v[222:225], v[22:25]
	v_mfma_f32_16x16x32_bf16 v[14:17], v[186:189], v[230:233], v[14:17]
	v_mfma_f32_16x16x32_bf16 v[10:13], v[194:197], v[230:233], v[10:13]
	s_setprio 0
	s_barrier
	s_add_i32 s29, s29, 2
	s_add_u32 s6, s6, 0x100
	s_addc_u32 s7, s7, 0
	s_cmp_gt_u32 s29, 29
	s_cbranch_scc0 .LBB0_1913
	s_and_b64 vcc, exec, s[24:25]
	s_cbranch_vccz .LBB0_1916
	s_barrier

.LBB0_1994:
	v_add_u32_e32 v147, s56, v163
	ds_read_b128 v[174:177], v147
	ds_read_b128 v[178:181], v147 offset:1024
	ds_read_b128 v[182:185], v147 offset:2048
	ds_read_b128 v[186:189], v147 offset:3072
	v_add_u32_e32 v147, s57, v163
	s_add_u32 s36, s84, s4
	ds_read_b128 v[190:193], v147
	ds_read_b128 v[194:197], v147 offset:1024
	ds_read_b128 v[198:201], v147 offset:2048
	ds_read_b128 v[202:205], v147 offset:3072
	s_addc_u32 s37, s85, s5
	s_add_u32 s60, s36, 0x29700100
	s_addc_u32 s61, s37, 0
	s_cmpk_eq_i32 s4, 0x700
	s_cselect_b64 vcc, -1, 0
	v_lshl_add_u64 v[206:207], v[158:159], 0, s[4:5]
	s_and_b64 s[36:37], vcc, exec
	v_cndmask_b32_e32 v136, v138, v141, vcc
	s_cselect_b32 s37, s9, s61
	s_cselect_b32 s36, s8, s60
	v_cndmask_b32_e32 v142, v150, v171, vcc
	v_cndmask_b32_e32 v214, v148, v172, vcc
	v_cndmask_b32_e32 v147, v152, v173, vcc
	v_cndmask_b32_e32 v243, v207, v145, vcc
	v_cndmask_b32_e32 v242, v206, v144, vcc
	v_lshl_add_u64 v[244:245], v[156:157], 0, s[4:5]
	s_add_i32 m0, s35, 0xc000
	ds_read_b128 v[206:209], v168
	ds_read_b128 v[210:213], v168 offset:1024
	ds_read_b128 v[218:221], v168 offset:2048
	ds_read_b128 v[222:225], v168 offset:3072
	ds_read_b128 v[226:229], v168 offset:4096
	ds_read_b128 v[230:233], v168 offset:5120
	ds_read_b128 v[234:237], v168 offset:6144
	ds_read_b128 v[238:241], v168 offset:7168
	global_load_lds_dwordx4 v[244:245], off
	v_lshl_add_u64 v[244:245], v[154:155], 0, s[4:5]
	s_add_i32 m0, s35, 0xe000
	s_nop 0
	global_load_lds_dwordx4 v[244:245], off
	s_waitcnt vmcnt(8)
	s_waitcnt lgkmcnt(0)
	s_barrier
	s_setprio 1
	s_waitcnt lgkmcnt(0)
	v_mfma_f32_16x16x32_bf16 v[126:129], v[174:177], v[206:209], v[126:129]
	v_mfma_f32_16x16x32_bf16 v[122:125], v[182:185], v[206:209], v[122:125]
	v_mfma_f32_16x16x32_bf16 v[110:113], v[174:177], v[218:221], v[110:113]
	v_mfma_f32_16x16x32_bf16 v[106:109], v[182:185], v[218:221], v[106:109]
	v_mfma_f32_16x16x32_bf16 v[94:97], v[174:177], v[226:229], v[94:97]
	v_mfma_f32_16x16x32_bf16 v[90:93], v[182:185], v[226:229], v[90:93]
	v_mfma_f32_16x16x32_bf16 v[78:81], v[174:177], v[234:237], v[78:81]
	v_mfma_f32_16x16x32_bf16 v[74:77], v[182:185], v[234:237], v[74:77]
	v_mfma_f32_16x16x32_bf16 v[126:129], v[178:181], v[210:213], v[126:129]
	v_mfma_f32_16x16x32_bf16 v[122:125], v[186:189], v[210:213], v[122:125]
	v_mfma_f32_16x16x32_bf16 v[110:113], v[178:181], v[222:225], v[110:113]
	v_mfma_f32_16x16x32_bf16 v[106:109], v[186:189], v[222:225], v[106:109]
	v_mfma_f32_16x16x32_bf16 v[94:97], v[178:181], v[230:233], v[94:97]
	v_mfma_f32_16x16x32_bf16 v[90:93], v[186:189], v[230:233], v[90:93]
	v_mfma_f32_16x16x32_bf16 v[78:81], v[178:181], v[238:241], v[78:81]
	v_mfma_f32_16x16x32_bf16 v[74:77], v[186:189], v[238:241], v[74:77]
	v_mfma_f32_16x16x32_bf16 v[118:121], v[190:193], v[206:209], v[118:121]
	v_mfma_f32_16x16x32_bf16 v[114:117], v[198:201], v[206:209], v[114:117]
	v_mfma_f32_16x16x32_bf16 v[102:105], v[190:193], v[218:221], v[102:105]
	v_mfma_f32_16x16x32_bf16 v[98:101], v[198:201], v[218:221], v[98:101]
	v_mfma_f32_16x16x32_bf16 v[86:89], v[190:193], v[226:229], v[86:89]
	v_mfma_f32_16x16x32_bf16 v[82:85], v[198:201], v[226:229], v[82:85]
	v_mfma_f32_16x16x32_bf16 v[70:73], v[190:193], v[234:237], v[70:73]
	v_mfma_f32_16x16x32_bf16 v[66:69], v[198:201], v[234:237], v[66:69]
	v_mfma_f32_16x16x32_bf16 v[118:121], v[194:197], v[210:213], v[118:121]
	v_mfma_f32_16x16x32_bf16 v[114:117], v[202:205], v[210:213], v[114:117]
	v_mfma_f32_16x16x32_bf16 v[102:105], v[194:197], v[222:225], v[102:105]
	v_mfma_f32_16x16x32_bf16 v[98:101], v[202:205], v[222:225], v[98:101]
	v_mfma_f32_16x16x32_bf16 v[86:89], v[194:197], v[230:233], v[86:89]
	v_mfma_f32_16x16x32_bf16 v[82:85], v[202:205], v[230:233], v[82:85]
	v_mfma_f32_16x16x32_bf16 v[70:73], v[194:197], v[238:241], v[70:73]
	v_mfma_f32_16x16x32_bf16 v[66:69], v[202:205], v[238:241], v[66:69]
	s_setprio 0
	s_barrier
	s_add_i32 s60, s56, s38
	v_lshl_add_u64 v[244:245], v[242:243], 0, v[132:133]
	s_mov_b32 m0, s60
	ds_read_b128 v[206:209], v168 offset:16384
	ds_read_b128 v[210:213], v168 offset:17408
	ds_read_b128 v[218:221], v168 offset:18432
	ds_read_b128 v[222:225], v168 offset:19456
	ds_read_b128 v[226:229], v168 offset:20480
	ds_read_b128 v[230:233], v168 offset:21504
	ds_read_b128 v[234:237], v168 offset:22528
	ds_read_b128 v[238:241], v168 offset:23552
	global_load_lds_dwordx4 v[244:245], off
	v_lshl_add_u64 v[246:247], v[242:243], 0, v[134:135]
	s_add_i32 m0, s60, 0x2000
	v_lshl_add_u64 v[248:249], v[242:243], 0, s[10:11]
	s_add_i32 s60, s57, s38
	global_load_lds_dwordx4 v[246:247], off
	v_lshl_add_u64 v[250:251], v[248:249], 0, v[132:133]
	s_mov_b32 m0, s60
	v_lshl_add_u64 v[248:249], v[248:249], 0, v[134:135]
	global_load_lds_dwordx4 v[250:251], off
	s_add_i32 m0, s60, 0x2000
	v_mov_b32_e32 v215, v137
	global_load_lds_dwordx4 v[248:249], off
	s_mov_b32 m0, s35
	v_lshl_add_u64 v[248:249], s[36:37], 0, v[136:137]
	global_load_lds_dwordx4 v136, s[36:37]
	s_mov_b32 m0, s39
	s_nop 0
	global_load_lds_dwordx4 v214, s[36:37]
	s_waitcnt vmcnt(8)
	s_waitcnt lgkmcnt(0)
	v_lshl_add_u64 v[214:215], s[36:37], 0, v[214:215]
	s_barrier
	s_setprio 1
	s_waitcnt lgkmcnt(0)
	v_mfma_f32_16x16x32_bf16 v[62:65], v[174:177], v[206:209], v[62:65]
	v_mfma_f32_16x16x32_bf16 v[58:61], v[182:185], v[206:209], v[58:61]
	v_mfma_f32_16x16x32_bf16 v[46:49], v[174:177], v[218:221], v[46:49]
	v_mfma_f32_16x16x32_bf16 v[42:45], v[182:185], v[218:221], v[42:45]
	v_mfma_f32_16x16x32_bf16 v[14:17], v[174:177], v[226:229], v[14:17]
	v_mfma_f32_16x16x32_bf16 v[10:13], v[182:185], v[226:229], v[10:13]
	v_mfma_f32_16x16x32_bf16 v[6:9], v[174:177], v[234:237], v[6:9]
	v_mfma_f32_16x16x32_bf16 v[2:5], v[182:185], v[234:237], v[2:5]
	v_mfma_f32_16x16x32_bf16 v[62:65], v[178:181], v[210:213], v[62:65]
	v_mfma_f32_16x16x32_bf16 v[58:61], v[186:189], v[210:213], v[58:61]
	v_mfma_f32_16x16x32_bf16 v[46:49], v[178:181], v[222:225], v[46:49]
	v_mfma_f32_16x16x32_bf16 v[42:45], v[186:189], v[222:225], v[42:45]
	v_mfma_f32_16x16x32_bf16 v[14:17], v[178:181], v[230:233], v[14:17]
	v_mfma_f32_16x16x32_bf16 v[10:13], v[186:189], v[230:233], v[10:13]
	v_mfma_f32_16x16x32_bf16 v[6:9], v[178:181], v[238:241], v[6:9]
	v_mfma_f32_16x16x32_bf16 v[2:5], v[186:189], v[238:241], v[2:5]
	v_mfma_f32_16x16x32_bf16 v[54:57], v[190:193], v[206:209], v[54:57]
	v_mfma_f32_16x16x32_bf16 v[50:53], v[198:201], v[206:209], v[50:53]
	v_mfma_f32_16x16x32_bf16 v[30:33], v[190:193], v[218:221], v[30:33]
	v_mfma_f32_16x16x32_bf16 v[26:29], v[198:201], v[218:221], v[26:29]
	v_mfma_f32_16x16x32_bf16 v[34:37], v[190:193], v[226:229], v[34:37]
	v_mfma_f32_16x16x32_bf16 v[38:41], v[198:201], v[226:229], v[38:41]
	v_mfma_f32_16x16x32_bf16 v[18:21], v[190:193], v[234:237], v[18:21]
	v_mfma_f32_16x16x32_bf16 v[22:25], v[198:201], v[234:237], v[22:25]
	v_mfma_f32_16x16x32_bf16 v[54:57], v[194:197], v[210:213], v[54:57]
	v_mfma_f32_16x16x32_bf16 v[50:53], v[202:205], v[210:213], v[50:53]
	v_mfma_f32_16x16x32_bf16 v[30:33], v[194:197], v[222:225], v[30:33]
	v_mfma_f32_16x16x32_bf16 v[26:29], v[202:205], v[222:225], v[26:29]
	v_mfma_f32_16x16x32_bf16 v[34:37], v[194:197], v[230:233], v[34:37]
	v_mfma_f32_16x16x32_bf16 v[38:41], v[202:205], v[230:233], v[38:41]
	v_mfma_f32_16x16x32_bf16 v[18:21], v[194:197], v[238:241], v[18:21]
	v_mfma_f32_16x16x32_bf16 v[22:25], v[202:205], v[238:241], v[22:25]
	s_setprio 0
	s_barrier
	s_add_i32 s60, 0, 0x18000
	v_add_u32_e32 v136, s60, v163
	s_add_i32 s61, 0, 0x1c000
	ds_read_b128 v[174:177], v136
	ds_read_b128 v[178:181], v136 offset:1024
	ds_read_b128 v[182:185], v136 offset:2048
	ds_read_b128 v[186:189], v136 offset:3072
	v_add_u32_e32 v136, s61, v163
	ds_read_b128 v[190:193], v136
	ds_read_b128 v[194:197], v136 offset:1024
	ds_read_b128 v[198:201], v136 offset:2048
	ds_read_b128 v[202:205], v136 offset:3072
	s_mov_b32 m0, s40
	ds_read_b128 v[206:209], v168 offset:32768
	ds_read_b128 v[210:213], v168 offset:33792
	ds_read_b128 v[218:221], v168 offset:34816
	ds_read_b128 v[222:225], v168 offset:35840
	ds_read_b128 v[226:229], v168 offset:36864
	ds_read_b128 v[230:233], v168 offset:37888
	ds_read_b128 v[234:237], v168 offset:38912
	ds_read_b128 v[238:241], v168 offset:39936
	global_load_lds_dwordx4 v142, s[36:37]
	s_mov_b32 m0, s41
	s_nop 0
	global_load_lds_dwordx4 v147, s[36:37]
	s_waitcnt vmcnt(8)
	s_waitcnt lgkmcnt(0)
	s_barrier
	s_setprio 1
	s_waitcnt lgkmcnt(0)
	v_mfma_f32_16x16x32_bf16 v[126:129], v[174:177], v[206:209], v[126:129]
	v_mfma_f32_16x16x32_bf16 v[122:125], v[182:185], v[206:209], v[122:125]
	v_mfma_f32_16x16x32_bf16 v[110:113], v[174:177], v[218:221], v[110:113]
	v_mfma_f32_16x16x32_bf16 v[106:109], v[182:185], v[218:221], v[106:109]
	v_mfma_f32_16x16x32_bf16 v[94:97], v[174:177], v[226:229], v[94:97]
	v_mfma_f32_16x16x32_bf16 v[90:93], v[182:185], v[226:229], v[90:93]
	v_mfma_f32_16x16x32_bf16 v[78:81], v[174:177], v[234:237], v[78:81]
	v_mfma_f32_16x16x32_bf16 v[74:77], v[182:185], v[234:237], v[74:77]
	v_mfma_f32_16x16x32_bf16 v[126:129], v[178:181], v[210:213], v[126:129]
	v_mfma_f32_16x16x32_bf16 v[122:125], v[186:189], v[210:213], v[122:125]
	v_mfma_f32_16x16x32_bf16 v[110:113], v[178:181], v[222:225], v[110:113]
	v_mfma_f32_16x16x32_bf16 v[106:109], v[186:189], v[222:225], v[106:109]
	v_mfma_f32_16x16x32_bf16 v[94:97], v[178:181], v[230:233], v[94:97]
	v_mfma_f32_16x16x32_bf16 v[90:93], v[186:189], v[230:233], v[90:93]
	v_mfma_f32_16x16x32_bf16 v[78:81], v[178:181], v[238:241], v[78:81]
	v_mfma_f32_16x16x32_bf16 v[74:77], v[186:189], v[238:241], v[74:77]
	v_mfma_f32_16x16x32_bf16 v[118:121], v[190:193], v[206:209], v[118:121]
	v_mfma_f32_16x16x32_bf16 v[114:117], v[198:201], v[206:209], v[114:117]
	v_mfma_f32_16x16x32_bf16 v[102:105], v[190:193], v[218:221], v[102:105]
	v_mfma_f32_16x16x32_bf16 v[98:101], v[198:201], v[218:221], v[98:101]
	v_mfma_f32_16x16x32_bf16 v[86:89], v[190:193], v[226:229], v[86:89]
	v_mfma_f32_16x16x32_bf16 v[82:85], v[198:201], v[226:229], v[82:85]
	v_mfma_f32_16x16x32_bf16 v[70:73], v[190:193], v[234:237], v[70:73]
	v_mfma_f32_16x16x32_bf16 v[66:69], v[198:201], v[234:237], v[66:69]
	v_mfma_f32_16x16x32_bf16 v[118:121], v[194:197], v[210:213], v[118:121]
	v_mfma_f32_16x16x32_bf16 v[114:117], v[202:205], v[210:213], v[114:117]
	v_mfma_f32_16x16x32_bf16 v[102:105], v[194:197], v[222:225], v[102:105]
	v_mfma_f32_16x16x32_bf16 v[98:101], v[202:205], v[222:225], v[98:101]
	v_mfma_f32_16x16x32_bf16 v[86:89], v[194:197], v[230:233], v[86:89]
	v_mfma_f32_16x16x32_bf16 v[82:85], v[202:205], v[230:233], v[82:85]
	v_mfma_f32_16x16x32_bf16 v[70:73], v[194:197], v[238:241], v[70:73]
	v_mfma_f32_16x16x32_bf16 v[66:69], v[202:205], v[238:241], v[66:69]
	s_setprio 0
	s_barrier
	s_add_i32 s36, s60, s38
	v_lshl_add_u64 v[244:245], v[244:245], 0, s[20:21]
	s_mov_b32 m0, s36
	ds_read_b128 v[206:209], v168 offset:49152
	ds_read_b128 v[210:213], v168 offset:50176
	ds_read_b128 v[218:221], v168 offset:51200
	ds_read_b128 v[222:225], v168 offset:52224
	ds_read_b128 v[226:229], v168 offset:53248
	ds_read_b128 v[230:233], v168 offset:54272
	ds_read_b128 v[234:237], v168 offset:55296
	ds_read_b128 v[238:241], v168 offset:56320
	global_load_lds_dwordx4 v[244:245], off
	v_lshl_add_u64 v[244:245], v[246:247], 0, s[20:21]
	s_add_i32 m0, s36, 0x2000
	v_lshl_add_u64 v[242:243], v[242:243], 0, s[24:25]
	s_add_i32 s36, s61, s38
	global_load_lds_dwordx4 v[244:245], off
	v_lshl_add_u64 v[244:245], v[242:243], 0, v[132:133]
	s_mov_b32 m0, s36
	v_lshl_add_u64 v[242:243], v[242:243], 0, v[134:135]
	global_load_lds_dwordx4 v[244:245], off
	s_add_i32 m0, s36, 0x2000
	v_lshl_add_u64 v[214:215], v[214:215], 0, s[20:21]
	global_load_lds_dwordx4 v[242:243], off
	v_lshl_add_u64 v[242:243], v[248:249], 0, s[20:21]
	s_mov_b32 m0, s43
	s_nop 0
	global_load_lds_dwordx4 v[242:243], off
	s_mov_b32 m0, s44
	s_nop 0
	global_load_lds_dwordx4 v[214:215], off
	s_waitcnt vmcnt(8)
	s_waitcnt lgkmcnt(0)
	s_barrier
	s_setprio 1
	s_waitcnt lgkmcnt(0)
	v_mfma_f32_16x16x32_bf16 v[62:65], v[174:177], v[206:209], v[62:65]
	v_mfma_f32_16x16x32_bf16 v[58:61], v[182:185], v[206:209], v[58:61]
	v_mfma_f32_16x16x32_bf16 v[46:49], v[174:177], v[218:221], v[46:49]
	v_mfma_f32_16x16x32_bf16 v[42:45], v[182:185], v[218:221], v[42:45]
	v_mfma_f32_16x16x32_bf16 v[14:17], v[174:177], v[226:229], v[14:17]
	v_mfma_f32_16x16x32_bf16 v[10:13], v[182:185], v[226:229], v[10:13]
	v_mfma_f32_16x16x32_bf16 v[6:9], v[174:177], v[234:237], v[6:9]
	v_mfma_f32_16x16x32_bf16 v[2:5], v[182:185], v[234:237], v[2:5]
	v_mfma_f32_16x16x32_bf16 v[62:65], v[178:181], v[210:213], v[62:65]
	v_mfma_f32_16x16x32_bf16 v[58:61], v[186:189], v[210:213], v[58:61]
	v_mfma_f32_16x16x32_bf16 v[46:49], v[178:181], v[222:225], v[46:49]
	v_mfma_f32_16x16x32_bf16 v[42:45], v[186:189], v[222:225], v[42:45]
	v_mfma_f32_16x16x32_bf16 v[14:17], v[178:181], v[230:233], v[14:17]
	v_mfma_f32_16x16x32_bf16 v[10:13], v[186:189], v[230:233], v[10:13]
	v_mfma_f32_16x16x32_bf16 v[6:9], v[178:181], v[238:241], v[6:9]
	v_mfma_f32_16x16x32_bf16 v[2:5], v[186:189], v[238:241], v[2:5]
	v_mfma_f32_16x16x32_bf16 v[54:57], v[190:193], v[206:209], v[54:57]
	v_mfma_f32_16x16x32_bf16 v[50:53], v[198:201], v[206:209], v[50:53]
	v_mfma_f32_16x16x32_bf16 v[30:33], v[190:193], v[218:221], v[30:33]
	v_mfma_f32_16x16x32_bf16 v[26:29], v[198:201], v[218:221], v[26:29]
	v_mfma_f32_16x16x32_bf16 v[34:37], v[190:193], v[226:229], v[34:37]
	v_mfma_f32_16x16x32_bf16 v[38:41], v[198:201], v[226:229], v[38:41]
	v_mfma_f32_16x16x32_bf16 v[18:21], v[190:193], v[234:237], v[18:21]
	v_mfma_f32_16x16x32_bf16 v[22:25], v[198:201], v[234:237], v[22:25]
	v_mfma_f32_16x16x32_bf16 v[54:57], v[194:197], v[210:213], v[54:57]
	v_mfma_f32_16x16x32_bf16 v[50:53], v[202:205], v[210:213], v[50:53]
	v_mfma_f32_16x16x32_bf16 v[30:33], v[194:197], v[222:225], v[30:33]
	v_mfma_f32_16x16x32_bf16 v[26:29], v[202:205], v[222:225], v[26:29]
	v_mfma_f32_16x16x32_bf16 v[34:37], v[194:197], v[230:233], v[34:37]
	v_mfma_f32_16x16x32_bf16 v[38:41], v[202:205], v[230:233], v[38:41]
	v_mfma_f32_16x16x32_bf16 v[18:21], v[194:197], v[238:241], v[18:21]
	v_mfma_f32_16x16x32_bf16 v[22:25], v[202:205], v[238:241], v[22:25]
	s_setprio 0
	s_barrier
	s_add_i32 s31, s31, 2
	s_add_u32 s4, s4, 0x100
	s_addc_u32 s5, s5, 0
	s_cmp_gt_u32 s31, 13
	s_cbranch_scc0 .LBB0_1994
	s_and_b64 vcc, exec, s[26:27]
	s_cbranch_vccz .LBB0_1997
	s_barrier
